# sc1 write-through on out-proj GEMM epilogue (Y) stores; UP loader index prologue de-serialized
# baseline (speedup 1.0000x reference)
; #define XG_ISSUE_B(pb_, t_) do { _Pragma("unroll") for (int j_ = 0; j_ < 8; ++j_) pb_[j_] = __builtin_bit_cast(f32x4, __builtin_amdgcn_raw_buffer_load_b128(rB, boff, (64 * (t_) + 8 * j_) * LDB * 4, 0)); } while (0)
; #define XG_ISSUE_A(pa_, t_) do { _Pragma("unroll") for (int j_ = 0; j_ < 8; ++j_) pa_[j_] = __builtin_amdgcn_raw_buffer_load_b128(rA, aoff[j_], 128 * (t_), 0); } while (0)
; #define XG_STORE(pb_, pa_, bo_) do { _Pragma("unroll") for (int j_ = 0; j_ < 8; ++j_) *(LAS v2u*)(lds + (bo_) + bdst + 8 * j_ * XG_BP) = pk4(pb_[j_]); \
;             _Pragma("unroll") for (int j_ = 0; j_ < 8; ++j_) *(LAS v4u*)(lds + (bo_) + (arow + 32 * j_) * XG_AP + ach * 16) = pa_[j_]; } while (0)
; template <bool UP>
; __device__ __forceinline__ void xgemm_unit(const Args& a, LAS unsigned char* lds, int e, int s, int cnt, int off_e, int rp, int tid, int lane, int wave) {
;     ...
;             const unsigned boff = (unsigned)(kr * LDB + 4 * n4 + (UP ? 64 : 128) * s) * 4u;
;             const int bdst = XG_ABYTES + kr * XG_BP + bcol * 2;
;             unsigned aoff[8];
; #pragma unroll
;             for (int j = 0; j < 8; ++j) { int rr = arow + 32 * j; rr = (rr < nrows) ? rr : (nrows - 1);
;                 if (UP) aoff[j] = ((unsigned)(LISTS[rp + rr] >> 1) * (unsigned)D + ach * 8) * 2u; else aoff[j] = ((unsigned)(off_e + rp + rr) * (unsigned)DE + ach * 8) * 2u; }
;             f32x4 pb0[8], pb1[8], pb2[8]; v4u pa0[8], pa1[8], pa2[8];
;             static_assert(NK % 3 == 2, "loader ring schedule");
;     ...
;             __builtin_amdgcn_s_setprio(1);
;             int ras_ = 0; float rw_ = 0.f;
;             if (!UP) ras_ = LISTS[rp + ((tl < nrows) ? tl : nrows - 1)];
;             XG_ISSUE_A(pa0, 0); XG_ISSUE_B(pb0, 0); XG_ISSUE_A(pa1, 1); XG_ISSUE_B(pb1, 1); XG_ISSUE_B(pb2, 2);
;             XG_STORE(pb0, pa0, 0);
;             __syncthreads();
.LBB0_1176:
	s_lshl_b32 s0, s12, 15
	s_add_u32 s0, s26, s0
	s_addc_u32 s1, s27, 0
	s_lshl_b32 s12, s12, 22
	s_add_u32 s12, s30, s12
	s_addc_u32 s13, s29, 0
	s_add_i32 s33, s33, -1
	s_and_b32 s13, s13, 0xffff
	v_min_i32_e32 v44, s33, v143
	v_min_i32_e32 v46, s33, v145
	v_min_i32_e32 v48, s33, v146
	v_min_i32_e32 v50, s33, v147
	v_min_i32_e32 v52, s33, v148
	v_min_i32_e32 v54, s33, v149
	v_min_i32_e32 v56, s33, v150
	v_min_i32_e32 v58, s33, v151
	v_add_u32_e32 v44, s3, v44
	v_add_u32_e32 v46, s3, v46
	v_add_u32_e32 v48, s3, v48
	v_add_u32_e32 v50, s3, v50
	v_add_u32_e32 v52, s3, v52
	v_add_u32_e32 v54, s3, v54
	v_add_u32_e32 v56, s3, v56
	v_add_u32_e32 v58, s3, v58
	v_ashrrev_i32_e32 v45, 31, v44
	v_ashrrev_i32_e32 v47, 31, v46
	v_ashrrev_i32_e32 v49, 31, v48
	v_ashrrev_i32_e32 v51, 31, v50
	v_ashrrev_i32_e32 v53, 31, v52
	v_ashrrev_i32_e32 v55, 31, v54
	v_ashrrev_i32_e32 v57, 31, v56
	v_ashrrev_i32_e32 v59, 31, v58
	v_lshl_add_u64 v[44:45], v[44:45], 2, s[0:1]
	v_lshl_add_u64 v[46:47], v[46:47], 2, s[0:1]
	v_lshl_add_u64 v[48:49], v[48:49], 2, s[0:1]
	v_lshl_add_u64 v[50:51], v[50:51], 2, s[0:1]
	v_lshl_add_u64 v[52:53], v[52:53], 2, s[0:1]
	v_lshl_add_u64 v[54:55], v[54:55], 2, s[0:1]
	v_lshl_add_u64 v[56:57], v[56:57], 2, s[0:1]
	v_lshl_add_u64 v[58:59], v[58:59], 2, s[0:1]
	global_load_dword v14, v[44:45], off
	global_load_dword v18, v[46:47], off
	global_load_dword v22, v[48:49], off
	global_load_dword v26, v[50:51], off
	global_load_dword v30, v[52:53], off
	global_load_dword v34, v[54:55], off
	global_load_dword v38, v[56:57], off
	global_load_dword v42, v[58:59], off
	s_waitcnt vmcnt(0)
	v_lshlrev_b32_e32 v14, 11, v14
	v_lshlrev_b32_e32 v18, 11, v18
	v_lshlrev_b32_e32 v22, 11, v22
	v_lshlrev_b32_e32 v26, 11, v26
	v_lshlrev_b32_e32 v30, 11, v30
	v_lshlrev_b32_e32 v34, 11, v34
	v_lshlrev_b32_e32 v38, 11, v38
	v_lshlrev_b32_e32 v42, 11, v42
	v_and_or_b32 v14, v14, s34, v144
	v_and_or_b32 v18, v18, s34, v144
	v_and_or_b32 v22, v22, s34, v144
	v_and_or_b32 v26, v26, s34, v144
	v_and_or_b32 v30, v30, s34, v144
	v_and_or_b32 v34, v34, s34, v144
	v_and_or_b32 v38, v38, s34, v144
	v_and_or_b32 v42, v42, s34, v144
	s_setprio 1
	v_lshl_or_b32 v2, s2, 8, v164
	buffer_load_dwordx4 v[4:7], v14, s[8:11], 0 offen
	buffer_load_dwordx4 v[8:11], v18, s[8:11], 0 offen
	buffer_load_dwordx4 v[44:47], v22, s[8:11], 0 offen
	buffer_load_dwordx4 v[48:51], v26, s[8:11], 0 offen
	buffer_load_dwordx4 v[52:55], v30, s[8:11], 0 offen
	buffer_load_dwordx4 v[56:59], v34, s[8:11], 0 offen
	buffer_load_dwordx4 v[60:63], v38, s[8:11], 0 offen
	buffer_load_dwordx4 v[64:67], v42, s[8:11], 0 offen
	buffer_load_dwordx4 v[68:71], v2, s[12:15], 0 offen
	s_movk_i32 s0, 0x4000
	buffer_load_dwordx4 v[72:75], v2, s[12:15], s0 offen
	s_mov_b32 s0, 0x8000
	buffer_load_dwordx4 v[76:79], v2, s[12:15], s0 offen
	s_mov_b32 s0, 0xc000
	buffer_load_dwordx4 v[80:83], v2, s[12:15], s0 offen
	s_mov_b32 s0, 0x10000
	buffer_load_dwordx4 v[84:87], v2, s[12:15], s0 offen
	s_mov_b32 s0, 0x14000
	buffer_load_dwordx4 v[88:91], v2, s[12:15], s0 offen
	s_mov_b32 s0, 0x18000
	buffer_load_dwordx4 v[92:95], v2, s[12:15], s0 offen
	s_mov_b32 s0, 0x1c000
	buffer_load_dwordx4 v[96:99], v2, s[12:15], s0 offen
	buffer_load_dwordx4 v[100:103], v14, s[8:11], s28 offen
	buffer_load_dwordx4 v[104:107], v18, s[8:11], s28 offen
	buffer_load_dwordx4 v[108:111], v22, s[8:11], s28 offen
	buffer_load_dwordx4 v[112:115], v26, s[8:11], s28 offen
	buffer_load_dwordx4 v[116:119], v30, s[8:11], s28 offen
	buffer_load_dwordx4 v[120:123], v34, s[8:11], s28 offen
	buffer_load_dwordx4 v[124:127], v38, s[8:11], s28 offen
	buffer_load_dwordx4 v[176:179], v42, s[8:11], s28 offen
	buffer_load_dwordx4 v[180:183], v2, s[12:15], s15 offen
	s_mov_b32 s0, 0x24000
	buffer_load_dwordx4 v[184:187], v2, s[12:15], s0 offen
	s_mov_b32 s0, 0x28000
	buffer_load_dwordx4 v[188:191], v2, s[12:15], s0 offen
	s_mov_b32 s0, 0x2c000
	buffer_load_dwordx4 v[192:195], v2, s[12:15], s0 offen
	s_mov_b32 s0, 0x30000
	buffer_load_dwordx4 v[196:199], v2, s[12:15], s0 offen
	s_mov_b32 s0, 0x34000
	buffer_load_dwordx4 v[200:203], v2, s[12:15], s0 offen
	s_mov_b32 s0, 0x38000
	buffer_load_dwordx4 v[204:207], v2, s[12:15], s0 offen
	s_mov_b32 s0, 0x3c000
	buffer_load_dwordx4 v[208:211], v2, s[12:15], s0 offen
	s_mov_b32 s0, 0x40000
	buffer_load_dwordx4 v[212:215], v2, s[12:15], s0 offen
	s_mov_b32 s0, 0x44000
	buffer_load_dwordx4 v[216:219], v2, s[12:15], s0 offen
	s_mov_b32 s0, 0x48000
	buffer_load_dwordx4 v[220:223], v2, s[12:15], s0 offen
	s_mov_b32 s0, 0x4c000
	buffer_load_dwordx4 v[224:227], v2, s[12:15], s0 offen
	s_mov_b32 s0, 0x50000
	buffer_load_dwordx4 v[228:231], v2, s[12:15], s0 offen
	s_mov_b32 s0, 0x54000
	buffer_load_dwordx4 v[232:235], v2, s[12:15], s0 offen
	s_mov_b32 s0, 0x58000
	buffer_load_dwordx4 v[236:239], v2, s[12:15], s0 offen
	s_mov_b32 s0, 0x5c000
	buffer_load_dwordx4 v[240:243], v2, s[12:15], s0 offen
	s_mov_b32 s0, 0x60000
	s_waitcnt vmcnt(31)
	v_cvt_pk_bf16_f32 v12, v68, v69
	v_cvt_pk_bf16_f32 v13, v70, v71
	ds_write_b64 v153, v[12:13] offset:40960
	s_waitcnt vmcnt(30)
	v_cvt_pk_bf16_f32 v12, v72, v73
	v_cvt_pk_bf16_f32 v13, v74, v75
	ds_write_b64 v153, v[12:13] offset:43136
	s_waitcnt vmcnt(29)
	v_cvt_pk_bf16_f32 v12, v76, v77
	v_cvt_pk_bf16_f32 v13, v78, v79
	ds_write_b64 v153, v[12:13] offset:45312
	s_waitcnt vmcnt(28)
	v_cvt_pk_bf16_f32 v12, v80, v81
	v_cvt_pk_bf16_f32 v13, v82, v83
	ds_write_b64 v153, v[12:13] offset:47488
	s_waitcnt vmcnt(27)
	v_cvt_pk_bf16_f32 v12, v84, v85
	v_cvt_pk_bf16_f32 v13, v86, v87
	ds_write_b64 v153, v[12:13] offset:49664
	s_waitcnt vmcnt(26)
	v_cvt_pk_bf16_f32 v12, v88, v89
	v_cvt_pk_bf16_f32 v13, v90, v91
	ds_write_b64 v153, v[12:13] offset:51840
	s_waitcnt vmcnt(25)
	v_cvt_pk_bf16_f32 v12, v92, v93
	v_cvt_pk_bf16_f32 v13, v94, v95
	ds_write_b64 v153, v[12:13] offset:54016
	s_waitcnt vmcnt(24)
	v_cvt_pk_bf16_f32 v12, v96, v97
	v_cvt_pk_bf16_f32 v13, v98, v99
	ds_write_b64 v153, v[12:13] offset:56192
	ds_write_b128 v165, v[4:7]
	ds_write_b128 v165, v[8:11] offset:5120
	ds_write_b128 v165, v[44:47] offset:10240
	ds_write_b128 v166, v[48:51]
	ds_write_b128 v165, v[52:55] offset:20480
	ds_write_b128 v165, v[56:59] offset:25600
	ds_write_b128 v165, v[60:63] offset:30720
	ds_write_b128 v167, v[64:67]
	s_waitcnt lgkmcnt(0)
	s_barrier
; #define XG_ISSUE_B(pb_, t_) do { _Pragma("unroll") for (int j_ = 0; j_ < 8; ++j_) pb_[j_] = __builtin_bit_cast(f32x4, __builtin_amdgcn_raw_buffer_load_b128(rB, boff, (64 * (t_) + 8 * j_) * LDB * 4, 0)); } while (0)
; #define XG_ISSUE_A(pa_, t_) do { _Pragma("unroll") for (int j_ = 0; j_ < 8; ++j_) pa_[j_] = __builtin_amdgcn_raw_buffer_load_b128(rA, aoff[j_], 128 * (t_), 0); } while (0)
; #define XG_STORE(pb_, pa_, bo_) do { _Pragma("unroll") for (int j_ = 0; j_ < 8; ++j_) *(LAS v2u*)(lds + (bo_) + bdst + 8 * j_ * XG_BP) = pk4(pb_[j_]); \
;             _Pragma("unroll") for (int j_ = 0; j_ < 8; ++j_) *(LAS v4u*)(lds + (bo_) + (arow + 32 * j_) * XG_AP + ach * 16) = pa_[j_]; } while (0)
; #define XG_STEP(t_, PBN, PAN, PBS, PAS) do { XG_ISSUE_A(PAN, (t_) + 2); { const int tb_ = ((t_) + 3 < NK) ? (t_) + 3 : NK - 1; XG_ISSUE_B(PBN, tb_); } \
;                 XG_STORE(PBS, PAS, (((t_) + 1) & 1) * XG_BUF); __syncthreads(); } while (0)
; template <bool UP>
; __device__ __forceinline__ void xgemm_unit(const Args& a, LAS unsigned char* lds, int e, int s, int cnt, int off_e, int rp, int tid, int lane, int wave) {
;     ...
;             __builtin_amdgcn_s_setprio(1);
;             int ras_ = 0; float rw_ = 0.f;
;             if (!UP) ras_ = LISTS[rp + ((tl < nrows) ? tl : nrows - 1)];
;             XG_ISSUE_A(pa0, 0); XG_ISSUE_B(pb0, 0); XG_ISSUE_A(pa1, 1); XG_ISSUE_B(pb1, 1); XG_ISSUE_B(pb2, 2);
;             XG_STORE(pb0, pa0, 0);
;             __syncthreads();
; #pragma unroll
;             for (int t = 0; t + 3 <= NK - 2; t += 3) {
;                 XG_STEP(t, pb0, pa2, pb1, pa1);
;                 if (!UP && t == 0) rw_ = RW[ras_];
;                 XG_STEP(t + 1, pb1, pa0, pb2, pa2);
;                 XG_STEP(t + 2, pb2, pa1, pb0, pa0);
	buffer_load_dwordx4 v[4:7], v14, s[8:11], s31 offen
	buffer_load_dwordx4 v[8:11], v18, s[8:11], s31 offen
	buffer_load_dwordx4 v[44:47], v22, s[8:11], s31 offen
	buffer_load_dwordx4 v[48:51], v26, s[8:11], s31 offen
	buffer_load_dwordx4 v[52:55], v30, s[8:11], s31 offen
	buffer_load_dwordx4 v[56:59], v34, s[8:11], s31 offen
	buffer_load_dwordx4 v[60:63], v38, s[8:11], s31 offen
	buffer_load_dwordx4 v[64:67], v42, s[8:11], s31 offen
	buffer_load_dwordx4 v[68:71], v2, s[12:15], s0 offen
	s_mov_b32 s0, 0x64000
	s_waitcnt vmcnt(24)
	v_cvt_pk_bf16_f32 v12, v180, v181
	v_cvt_pk_bf16_f32 v13, v182, v183
	buffer_load_dwordx4 v[72:75], v2, s[12:15], s0 offen
	s_mov_b32 s0, 0x68000
	ds_write_b64 v154, v[12:13] offset:58368
	s_waitcnt vmcnt(24)
	v_cvt_pk_bf16_f32 v12, v184, v185
	v_cvt_pk_bf16_f32 v13, v186, v187
	buffer_load_dwordx4 v[76:79], v2, s[12:15], s0 offen
	s_mov_b32 s0, 0x6c000
	ds_write_b64 v154, v[12:13] offset:60544
	s_waitcnt vmcnt(24)
	v_cvt_pk_bf16_f32 v12, v188, v189
	v_cvt_pk_bf16_f32 v13, v190, v191
	buffer_load_dwordx4 v[80:83], v2, s[12:15], s0 offen
	s_mov_b32 s0, 0x70000
	ds_write_b64 v154, v[12:13] offset:62720
	s_waitcnt vmcnt(24)
	v_cvt_pk_bf16_f32 v12, v192, v193
	v_cvt_pk_bf16_f32 v13, v194, v195
	buffer_load_dwordx4 v[84:87], v2, s[12:15], s0 offen
	s_mov_b32 s0, 0x74000
	ds_write_b64 v154, v[12:13] offset:64896
	s_waitcnt vmcnt(24)
	v_cvt_pk_bf16_f32 v12, v196, v197
	v_cvt_pk_bf16_f32 v13, v198, v199
	buffer_load_dwordx4 v[88:91], v2, s[12:15], s0 offen
	s_mov_b32 s0, 0x78000
	ds_write_b64 v155, v[12:13]
	s_waitcnt vmcnt(24)
	v_cvt_pk_bf16_f32 v12, v200, v201
	v_cvt_pk_bf16_f32 v13, v202, v203
	buffer_load_dwordx4 v[92:95], v2, s[12:15], s0 offen
	s_mov_b32 s0, 0x7c000
	ds_write_b64 v156, v[12:13]
	s_waitcnt vmcnt(24)
	v_cvt_pk_bf16_f32 v12, v204, v205
	v_cvt_pk_bf16_f32 v13, v206, v207
	buffer_load_dwordx4 v[96:99], v2, s[12:15], s0 offen
	ds_write_b64 v157, v[12:13]
	s_waitcnt vmcnt(24)
	v_cvt_pk_bf16_f32 v12, v208, v209
	v_cvt_pk_bf16_f32 v13, v210, v211
	ds_write_b64 v158, v[12:13]
	ds_write_b128 v165, v[100:103] offset:58368
	ds_write_b128 v165, v[104:107] offset:63488
	ds_write_b128 v168, v[108:111] offset:58368
	ds_write_b128 v166, v[112:115] offset:58368
	ds_write_b128 v169, v[116:119] offset:58368
	ds_write_b128 v169, v[120:123] offset:63488
	ds_write_b128 v170, v[124:127] offset:63488
	ds_write_b128 v167, v[176:179] offset:58368
	s_waitcnt lgkmcnt(0)
	s_barrier
	buffer_load_dwordx4 v[100:103], v14, s[8:11], s35 offen
	buffer_load_dwordx4 v[104:107], v18, s[8:11], s35 offen
	buffer_load_dwordx4 v[108:111], v22, s[8:11], s35 offen
	buffer_load_dwordx4 v[112:115], v26, s[8:11], s35 offen
	buffer_load_dwordx4 v[116:119], v30, s[8:11], s35 offen
	buffer_load_dwordx4 v[120:123], v34, s[8:11], s35 offen
	buffer_load_dwordx4 v[124:127], v38, s[8:11], s35 offen
	buffer_load_dwordx4 v[176:179], v42, s[8:11], s35 offen
	s_mov_b32 s0, 0x80000
	buffer_load_dwordx4 v[180:183], v2, s[12:15], s0 offen
	s_mov_b32 s0, 0x84000
	s_waitcnt vmcnt(32)
	v_cvt_pk_bf16_f32 v12, v212, v213
	v_cvt_pk_bf16_f32 v13, v214, v215
	buffer_load_dwordx4 v[184:187], v2, s[12:15], s0 offen
	s_mov_b32 s0, 0x88000
	ds_write_b64 v153, v[12:13] offset:40960
	s_waitcnt vmcnt(32)
	v_cvt_pk_bf16_f32 v12, v216, v217
	v_cvt_pk_bf16_f32 v13, v218, v219
	buffer_load_dwordx4 v[188:191], v2, s[12:15], s0 offen
	s_mov_b32 s0, 0x8c000
	ds_write_b64 v153, v[12:13] offset:43136
	s_waitcnt vmcnt(32)
	v_cvt_pk_bf16_f32 v12, v220, v221
	v_cvt_pk_bf16_f32 v13, v222, v223
	buffer_load_dwordx4 v[192:195], v2, s[12:15], s0 offen
	s_mov_b32 s0, 0x90000
	ds_write_b64 v153, v[12:13] offset:45312
	s_waitcnt vmcnt(32)
	v_cvt_pk_bf16_f32 v12, v224, v225
	v_cvt_pk_bf16_f32 v13, v226, v227
	buffer_load_dwordx4 v[196:199], v2, s[12:15], s0 offen
	s_mov_b32 s0, 0x94000
	ds_write_b64 v153, v[12:13] offset:47488
	s_waitcnt vmcnt(32)
	v_cvt_pk_bf16_f32 v12, v228, v229
	v_cvt_pk_bf16_f32 v13, v230, v231
	buffer_load_dwordx4 v[200:203], v2, s[12:15], s0 offen
	s_mov_b32 s0, 0x98000
	ds_write_b64 v153, v[12:13] offset:49664
	s_waitcnt vmcnt(32)
	v_cvt_pk_bf16_f32 v12, v232, v233
	v_cvt_pk_bf16_f32 v13, v234, v235
	buffer_load_dwordx4 v[204:207], v2, s[12:15], s0 offen
	s_mov_b32 s0, 0x9c000
	ds_write_b64 v153, v[12:13] offset:51840
	s_waitcnt vmcnt(32)
	v_cvt_pk_bf16_f32 v12, v236, v237
	v_cvt_pk_bf16_f32 v13, v238, v239
	buffer_load_dwordx4 v[208:211], v2, s[12:15], s0 offen
	ds_write_b64 v153, v[12:13] offset:54016
	s_waitcnt vmcnt(32)
	v_cvt_pk_bf16_f32 v12, v240, v241
	v_cvt_pk_bf16_f32 v13, v242, v243
	ds_write_b64 v153, v[12:13] offset:56192
	s_waitcnt vmcnt(31)
	ds_write_b128 v165, v[4:7]
	s_waitcnt vmcnt(30)
	ds_write_b128 v165, v[8:11] offset:5120
	s_waitcnt vmcnt(29)
	ds_write_b128 v165, v[44:47] offset:10240
	s_waitcnt vmcnt(28)
	ds_write_b128 v166, v[48:51]
	s_waitcnt vmcnt(27)
	ds_write_b128 v165, v[52:55] offset:20480
	s_waitcnt vmcnt(26)
	ds_write_b128 v165, v[56:59] offset:25600
	s_waitcnt vmcnt(25)
	ds_write_b128 v165, v[60:63] offset:30720
	s_waitcnt vmcnt(24)
	ds_write_b128 v167, v[64:67]
	s_waitcnt lgkmcnt(0)
	s_barrier
; #define XG_ISSUE_B(pb_, t_) do { _Pragma("unroll") for (int j_ = 0; j_ < 8; ++j_) pb_[j_] = __builtin_bit_cast(f32x4, __builtin_amdgcn_raw_buffer_load_b128(rB, boff, (64 * (t_) + 8 * j_) * LDB * 4, 0)); } while (0)
; #define XG_ISSUE_A(pa_, t_) do { _Pragma("unroll") for (int j_ = 0; j_ < 8; ++j_) pa_[j_] = __builtin_amdgcn_raw_buffer_load_b128(rA, aoff[j_], 128 * (t_), 0); } while (0)
; #define XG_STORE(pb_, pa_, bo_) do { _Pragma("unroll") for (int j_ = 0; j_ < 8; ++j_) *(LAS v2u*)(lds + (bo_) + bdst + 8 * j_ * XG_BP) = pk4(pb_[j_]); \
;             _Pragma("unroll") for (int j_ = 0; j_ < 8; ++j_) *(LAS v4u*)(lds + (bo_) + (arow + 32 * j_) * XG_AP + ach * 16) = pa_[j_]; } while (0)
; #define XG_STEP(t_, PBN, PAN, PBS, PAS) do { XG_ISSUE_A(PAN, (t_) + 2); { const int tb_ = ((t_) + 3 < NK) ? (t_) + 3 : NK - 1; XG_ISSUE_B(PBN, tb_); } \
;                 XG_STORE(PBS, PAS, (((t_) + 1) & 1) * XG_BUF); __syncthreads(); } while (0)
; template <bool UP>
; __device__ __forceinline__ void xgemm_unit(const Args& a, LAS unsigned char* lds, int e, int s, int cnt, int off_e, int rp, int tid, int lane, int wave) {
;     ...
;             __builtin_amdgcn_s_setprio(1);
;             int ras_ = 0; float rw_ = 0.f;
;             if (!UP) ras_ = LISTS[rp + ((tl < nrows) ? tl : nrows - 1)];
;             XG_ISSUE_A(pa0, 0); XG_ISSUE_B(pb0, 0); XG_ISSUE_A(pa1, 1); XG_ISSUE_B(pb1, 1); XG_ISSUE_B(pb2, 2);
;             XG_STORE(pb0, pa0, 0);
;             __syncthreads();
; #pragma unroll
;             for (int t = 0; t + 3 <= NK - 2; t += 3) {
;                 XG_STEP(t, pb0, pa2, pb1, pa1);
;                 if (!UP && t == 0) rw_ = RW[ras_];
;                 XG_STEP(t + 1, pb1, pa0, pb2, pa2);
;                 XG_STEP(t + 2, pb2, pa1, pb0, pa0);
	buffer_load_dwordx4 v[4:7], v14, s[8:11], s36 offen
	buffer_load_dwordx4 v[8:11], v18, s[8:11], s36 offen
	buffer_load_dwordx4 v[44:47], v22, s[8:11], s36 offen
	buffer_load_dwordx4 v[48:51], v26, s[8:11], s36 offen
	buffer_load_dwordx4 v[52:55], v30, s[8:11], s36 offen
	buffer_load_dwordx4 v[56:59], v34, s[8:11], s36 offen
	buffer_load_dwordx4 v[60:63], v38, s[8:11], s36 offen
	buffer_load_dwordx4 v[64:67], v42, s[8:11], s36 offen
	s_mov_b32 s0, 0xa0000
	buffer_load_dwordx4 v[212:215], v2, s[12:15], s0 offen
	s_mov_b32 s0, 0xa4000
	s_waitcnt vmcnt(32)
	v_cvt_pk_bf16_f32 v12, v68, v69
	v_cvt_pk_bf16_f32 v13, v70, v71
	buffer_load_dwordx4 v[216:219], v2, s[12:15], s0 offen
	s_mov_b32 s0, 0xa8000
	ds_write_b64 v154, v[12:13] offset:58368
	s_waitcnt vmcnt(32)
	v_cvt_pk_bf16_f32 v12, v72, v73
	v_cvt_pk_bf16_f32 v13, v74, v75
	buffer_load_dwordx4 v[220:223], v2, s[12:15], s0 offen
	s_mov_b32 s0, 0xac000
	ds_write_b64 v154, v[12:13] offset:60544
	s_waitcnt vmcnt(32)
	v_cvt_pk_bf16_f32 v12, v76, v77
	v_cvt_pk_bf16_f32 v13, v78, v79
	buffer_load_dwordx4 v[224:227], v2, s[12:15], s0 offen
	s_mov_b32 s0, 0xb0000
	ds_write_b64 v154, v[12:13] offset:62720
	s_waitcnt vmcnt(32)
	v_cvt_pk_bf16_f32 v12, v80, v81
	v_cvt_pk_bf16_f32 v13, v82, v83
	buffer_load_dwordx4 v[228:231], v2, s[12:15], s0 offen
	s_mov_b32 s0, 0xb4000
	ds_write_b64 v154, v[12:13] offset:64896
	s_waitcnt vmcnt(32)
	v_cvt_pk_bf16_f32 v12, v84, v85
	v_cvt_pk_bf16_f32 v13, v86, v87
	buffer_load_dwordx4 v[232:235], v2, s[12:15], s0 offen
	s_mov_b32 s0, 0xb8000
	ds_write_b64 v155, v[12:13]
	s_waitcnt vmcnt(32)
	v_cvt_pk_bf16_f32 v12, v88, v89
	v_cvt_pk_bf16_f32 v13, v90, v91
	buffer_load_dwordx4 v[236:239], v2, s[12:15], s0 offen
	s_mov_b32 s0, 0xbc000
	ds_write_b64 v156, v[12:13]
	s_waitcnt vmcnt(32)
	v_cvt_pk_bf16_f32 v12, v92, v93
	v_cvt_pk_bf16_f32 v13, v94, v95
	buffer_load_dwordx4 v[240:243], v2, s[12:15], s0 offen
	ds_write_b64 v157, v[12:13]
	s_waitcnt vmcnt(32)
	v_cvt_pk_bf16_f32 v12, v96, v97
	v_cvt_pk_bf16_f32 v13, v98, v99
	ds_write_b64 v158, v[12:13]
	s_waitcnt vmcnt(31)
	ds_write_b128 v165, v[100:103] offset:58368
	s_waitcnt vmcnt(30)
	ds_write_b128 v165, v[104:107] offset:63488
	s_waitcnt vmcnt(29)
	ds_write_b128 v168, v[108:111] offset:58368
	s_waitcnt vmcnt(28)
	ds_write_b128 v166, v[112:115] offset:58368
	s_waitcnt vmcnt(27)
	ds_write_b128 v169, v[116:119] offset:58368
	s_waitcnt vmcnt(26)
	ds_write_b128 v169, v[120:123] offset:63488
	s_waitcnt vmcnt(25)
	ds_write_b128 v170, v[124:127] offset:63488
	s_waitcnt vmcnt(24)
	ds_write_b128 v167, v[176:179] offset:58368
	s_waitcnt lgkmcnt(0)
	s_barrier
	buffer_load_dwordx4 v[68:71], v14, s[8:11], s37 offen
	buffer_load_dwordx4 v[72:75], v18, s[8:11], s37 offen
	buffer_load_dwordx4 v[76:79], v22, s[8:11], s37 offen
	buffer_load_dwordx4 v[80:83], v26, s[8:11], s37 offen
	buffer_load_dwordx4 v[84:87], v30, s[8:11], s37 offen
	buffer_load_dwordx4 v[88:91], v34, s[8:11], s37 offen
	buffer_load_dwordx4 v[92:95], v38, s[8:11], s37 offen
	buffer_load_dwordx4 v[96:99], v42, s[8:11], s37 offen
	s_mov_b32 s0, 0xc0000
	buffer_load_dwordx4 v[100:103], v2, s[12:15], s0 offen
	s_mov_b32 s0, 0xc4000
	s_waitcnt vmcnt(32)
	v_cvt_pk_bf16_f32 v12, v180, v181
	v_cvt_pk_bf16_f32 v13, v182, v183
	buffer_load_dwordx4 v[104:107], v2, s[12:15], s0 offen
	s_mov_b32 s0, 0xc8000
	ds_write_b64 v153, v[12:13] offset:40960
	s_waitcnt vmcnt(32)
	v_cvt_pk_bf16_f32 v12, v184, v185
	v_cvt_pk_bf16_f32 v13, v186, v187
	buffer_load_dwordx4 v[108:111], v2, s[12:15], s0 offen
	s_mov_b32 s0, 0xcc000
	ds_write_b64 v153, v[12:13] offset:43136
	s_waitcnt vmcnt(32)
	v_cvt_pk_bf16_f32 v12, v188, v189
	v_cvt_pk_bf16_f32 v13, v190, v191
	buffer_load_dwordx4 v[112:115], v2, s[12:15], s0 offen
	s_mov_b32 s0, 0xd0000
	ds_write_b64 v153, v[12:13] offset:45312
	s_waitcnt vmcnt(32)
	v_cvt_pk_bf16_f32 v12, v192, v193
	v_cvt_pk_bf16_f32 v13, v194, v195
	buffer_load_dwordx4 v[116:119], v2, s[12:15], s0 offen
	s_mov_b32 s0, 0xd4000
	ds_write_b64 v153, v[12:13] offset:47488
	s_waitcnt vmcnt(32)
	v_cvt_pk_bf16_f32 v12, v196, v197
	v_cvt_pk_bf16_f32 v13, v198, v199
	buffer_load_dwordx4 v[120:123], v2, s[12:15], s0 offen
	s_mov_b32 s0, 0xd8000
	ds_write_b64 v153, v[12:13] offset:49664
	s_waitcnt vmcnt(32)
	v_cvt_pk_bf16_f32 v12, v200, v201
	v_cvt_pk_bf16_f32 v13, v202, v203
	buffer_load_dwordx4 v[124:127], v2, s[12:15], s0 offen
	s_mov_b32 s0, 0xdc000
	ds_write_b64 v153, v[12:13] offset:51840
	s_waitcnt vmcnt(32)
	v_cvt_pk_bf16_f32 v12, v204, v205
	v_cvt_pk_bf16_f32 v13, v206, v207
	buffer_load_dwordx4 v[176:179], v2, s[12:15], s0 offen
	ds_write_b64 v153, v[12:13] offset:54016
	s_waitcnt vmcnt(32)
	v_cvt_pk_bf16_f32 v12, v208, v209
	v_cvt_pk_bf16_f32 v13, v210, v211
	ds_write_b64 v153, v[12:13] offset:56192
	s_waitcnt vmcnt(31)
	ds_write_b128 v165, v[4:7]
	s_waitcnt vmcnt(30)
	ds_write_b128 v165, v[8:11] offset:5120
	s_waitcnt vmcnt(29)
	ds_write_b128 v165, v[44:47] offset:10240
	s_waitcnt vmcnt(28)
	ds_write_b128 v166, v[48:51]
	s_waitcnt vmcnt(27)
	ds_write_b128 v165, v[52:55] offset:20480
	s_waitcnt vmcnt(26)
	ds_write_b128 v165, v[56:59] offset:25600
	s_waitcnt vmcnt(25)
	ds_write_b128 v165, v[60:63] offset:30720
	s_waitcnt vmcnt(24)
	ds_write_b128 v167, v[64:67]
	s_waitcnt lgkmcnt(0)
	s_barrier
; #define XG_ISSUE_B(pb_, t_) do { _Pragma("unroll") for (int j_ = 0; j_ < 8; ++j_) pb_[j_] = __builtin_bit_cast(f32x4, __builtin_amdgcn_raw_buffer_load_b128(rB, boff, (64 * (t_) + 8 * j_) * LDB * 4, 0)); } while (0)
; #define XG_ISSUE_A(pa_, t_) do { _Pragma("unroll") for (int j_ = 0; j_ < 8; ++j_) pa_[j_] = __builtin_amdgcn_raw_buffer_load_b128(rA, aoff[j_], 128 * (t_), 0); } while (0)
; #define XG_STORE(pb_, pa_, bo_) do { _Pragma("unroll") for (int j_ = 0; j_ < 8; ++j_) *(LAS v2u*)(lds + (bo_) + bdst + 8 * j_ * XG_BP) = pk4(pb_[j_]); \
;             _Pragma("unroll") for (int j_ = 0; j_ < 8; ++j_) *(LAS v4u*)(lds + (bo_) + (arow + 32 * j_) * XG_AP + ach * 16) = pa_[j_]; } while (0)
; #define XG_STEP(t_, PBN, PAN, PBS, PAS) do { XG_ISSUE_A(PAN, (t_) + 2); { const int tb_ = ((t_) + 3 < NK) ? (t_) + 3 : NK - 1; XG_ISSUE_B(PBN, tb_); } \
;                 XG_STORE(PBS, PAS, (((t_) + 1) & 1) * XG_BUF); __syncthreads(); } while (0)
; template <bool UP>
; __device__ __forceinline__ void xgemm_unit(const Args& a, LAS unsigned char* lds, int e, int s, int cnt, int off_e, int rp, int tid, int lane, int wave) {
;     ...
;             __builtin_amdgcn_s_setprio(1);
;             int ras_ = 0; float rw_ = 0.f;
;             if (!UP) ras_ = LISTS[rp + ((tl < nrows) ? tl : nrows - 1)];
;             XG_ISSUE_A(pa0, 0); XG_ISSUE_B(pb0, 0); XG_ISSUE_A(pa1, 1); XG_ISSUE_B(pb1, 1); XG_ISSUE_B(pb2, 2);
;             XG_STORE(pb0, pa0, 0);
;             __syncthreads();
; #pragma unroll
;             for (int t = 0; t + 3 <= NK - 2; t += 3) {
;                 XG_STEP(t, pb0, pa2, pb1, pa1);
;                 if (!UP && t == 0) rw_ = RW[ras_];
;                 XG_STEP(t + 1, pb1, pa0, pb2, pa2);
;                 XG_STEP(t + 2, pb2, pa1, pb0, pa0);
	buffer_load_dwordx4 v[4:7], v14, s[8:11], s38 offen
	buffer_load_dwordx4 v[8:11], v18, s[8:11], s38 offen
	buffer_load_dwordx4 v[44:47], v22, s[8:11], s38 offen
	buffer_load_dwordx4 v[48:51], v26, s[8:11], s38 offen
	buffer_load_dwordx4 v[52:55], v30, s[8:11], s38 offen
	buffer_load_dwordx4 v[56:59], v34, s[8:11], s38 offen
	buffer_load_dwordx4 v[60:63], v38, s[8:11], s38 offen
	buffer_load_dwordx4 v[64:67], v42, s[8:11], s38 offen
	s_mov_b32 s0, 0xe0000
	buffer_load_dwordx4 v[180:183], v2, s[12:15], s0 offen
	s_mov_b32 s0, 0xe4000
	s_waitcnt vmcnt(32)
	v_cvt_pk_bf16_f32 v12, v212, v213
	v_cvt_pk_bf16_f32 v13, v214, v215
	buffer_load_dwordx4 v[184:187], v2, s[12:15], s0 offen
	s_mov_b32 s0, 0xe8000
	ds_write_b64 v154, v[12:13] offset:58368
	s_waitcnt vmcnt(32)
	v_cvt_pk_bf16_f32 v12, v216, v217
	v_cvt_pk_bf16_f32 v13, v218, v219
	buffer_load_dwordx4 v[188:191], v2, s[12:15], s0 offen
	s_mov_b32 s0, 0xec000
	ds_write_b64 v154, v[12:13] offset:60544
	s_waitcnt vmcnt(32)
	v_cvt_pk_bf16_f32 v12, v220, v221
	v_cvt_pk_bf16_f32 v13, v222, v223
	buffer_load_dwordx4 v[192:195], v2, s[12:15], s0 offen
	s_mov_b32 s0, 0xf0000
	ds_write_b64 v154, v[12:13] offset:62720
	s_waitcnt vmcnt(32)
	v_cvt_pk_bf16_f32 v12, v224, v225
	v_cvt_pk_bf16_f32 v13, v226, v227
	buffer_load_dwordx4 v[196:199], v2, s[12:15], s0 offen
	s_mov_b32 s0, 0xf4000
	ds_write_b64 v154, v[12:13] offset:64896
	s_waitcnt vmcnt(32)
	v_cvt_pk_bf16_f32 v12, v228, v229
	v_cvt_pk_bf16_f32 v13, v230, v231
	buffer_load_dwordx4 v[200:203], v2, s[12:15], s0 offen
	s_mov_b32 s0, 0xf8000
	ds_write_b64 v155, v[12:13]
	s_waitcnt vmcnt(32)
	v_cvt_pk_bf16_f32 v12, v232, v233
	v_cvt_pk_bf16_f32 v13, v234, v235
	buffer_load_dwordx4 v[204:207], v2, s[12:15], s0 offen
	s_mov_b32 s0, 0xfc000
	ds_write_b64 v156, v[12:13]
	s_waitcnt vmcnt(32)
	v_cvt_pk_bf16_f32 v12, v236, v237
	v_cvt_pk_bf16_f32 v13, v238, v239
	buffer_load_dwordx4 v[208:211], v2, s[12:15], s0 offen
	ds_write_b64 v157, v[12:13]
	s_waitcnt vmcnt(32)
	v_cvt_pk_bf16_f32 v12, v240, v241
	v_cvt_pk_bf16_f32 v13, v242, v243
	ds_write_b64 v158, v[12:13]
	s_waitcnt vmcnt(31)
	ds_write_b128 v165, v[68:71] offset:58368
	s_waitcnt vmcnt(30)
	ds_write_b128 v165, v[72:75] offset:63488
	s_waitcnt vmcnt(29)
	ds_write_b128 v168, v[76:79] offset:58368
	s_waitcnt vmcnt(28)
	ds_write_b128 v166, v[80:83] offset:58368
	s_waitcnt vmcnt(27)
	ds_write_b128 v169, v[84:87] offset:58368
	s_waitcnt vmcnt(26)
	ds_write_b128 v169, v[88:91] offset:63488
	s_waitcnt vmcnt(25)
	ds_write_b128 v170, v[92:95] offset:63488
	s_waitcnt vmcnt(24)
	ds_write_b128 v167, v[96:99] offset:58368
	s_waitcnt lgkmcnt(0)
	s_barrier
	buffer_load_dwordx4 v[68:71], v14, s[8:11], s39 offen
	buffer_load_dwordx4 v[72:75], v18, s[8:11], s39 offen
	buffer_load_dwordx4 v[76:79], v22, s[8:11], s39 offen
	buffer_load_dwordx4 v[80:83], v26, s[8:11], s39 offen
	buffer_load_dwordx4 v[84:87], v30, s[8:11], s39 offen
	buffer_load_dwordx4 v[88:91], v34, s[8:11], s39 offen
	buffer_load_dwordx4 v[92:95], v38, s[8:11], s39 offen
	buffer_load_dwordx4 v[96:99], v42, s[8:11], s39 offen
	s_mov_b32 s0, 0x100000
	buffer_load_dwordx4 v[212:215], v2, s[12:15], s0 offen
	s_mov_b32 s0, 0x104000
	s_waitcnt vmcnt(32)
	v_cvt_pk_bf16_f32 v12, v100, v101
	v_cvt_pk_bf16_f32 v13, v102, v103
	buffer_load_dwordx4 v[216:219], v2, s[12:15], s0 offen
	s_mov_b32 s0, 0x108000
	ds_write_b64 v153, v[12:13] offset:40960
	s_waitcnt vmcnt(32)
	v_cvt_pk_bf16_f32 v12, v104, v105
	v_cvt_pk_bf16_f32 v13, v106, v107
	buffer_load_dwordx4 v[220:223], v2, s[12:15], s0 offen
	s_mov_b32 s0, 0x10c000
	ds_write_b64 v153, v[12:13] offset:43136
	s_waitcnt vmcnt(32)
	v_cvt_pk_bf16_f32 v12, v108, v109
	v_cvt_pk_bf16_f32 v13, v110, v111
	buffer_load_dwordx4 v[224:227], v2, s[12:15], s0 offen
	s_mov_b32 s0, 0x110000
	ds_write_b64 v153, v[12:13] offset:45312
	s_waitcnt vmcnt(32)
	v_cvt_pk_bf16_f32 v12, v112, v113
	v_cvt_pk_bf16_f32 v13, v114, v115
	buffer_load_dwordx4 v[228:231], v2, s[12:15], s0 offen
	s_mov_b32 s0, 0x114000
	ds_write_b64 v153, v[12:13] offset:47488
	s_waitcnt vmcnt(32)
	v_cvt_pk_bf16_f32 v12, v116, v117
	v_cvt_pk_bf16_f32 v13, v118, v119
	buffer_load_dwordx4 v[232:235], v2, s[12:15], s0 offen
	s_mov_b32 s0, 0x118000
	ds_write_b64 v153, v[12:13] offset:49664
	s_waitcnt vmcnt(32)
	v_cvt_pk_bf16_f32 v12, v120, v121
	v_cvt_pk_bf16_f32 v13, v122, v123
	buffer_load_dwordx4 v[236:239], v2, s[12:15], s0 offen
	s_mov_b32 s0, 0x11c000
	ds_write_b64 v153, v[12:13] offset:51840
	s_waitcnt vmcnt(32)
	v_cvt_pk_bf16_f32 v12, v124, v125
	v_cvt_pk_bf16_f32 v13, v126, v127
	buffer_load_dwordx4 v[240:243], v2, s[12:15], s0 offen
	ds_write_b64 v153, v[12:13] offset:54016
	s_waitcnt vmcnt(32)
	v_cvt_pk_bf16_f32 v12, v176, v177
	v_cvt_pk_bf16_f32 v13, v178, v179
	ds_write_b64 v153, v[12:13] offset:56192
	s_waitcnt vmcnt(31)
	ds_write_b128 v165, v[4:7]
	s_waitcnt vmcnt(30)
	ds_write_b128 v165, v[8:11] offset:5120
	s_waitcnt vmcnt(29)
	ds_write_b128 v165, v[44:47] offset:10240
	s_waitcnt vmcnt(28)
	ds_write_b128 v166, v[48:51]
	s_waitcnt vmcnt(27)
	ds_write_b128 v165, v[52:55] offset:20480
	s_waitcnt vmcnt(26)
	ds_write_b128 v165, v[56:59] offset:25600
	s_waitcnt vmcnt(25)
	ds_write_b128 v165, v[60:63] offset:30720
	s_waitcnt vmcnt(24)
	ds_write_b128 v167, v[64:67]
	s_waitcnt lgkmcnt(0)
	s_barrier
; #define XG_ISSUE_B(pb_, t_) do { _Pragma("unroll") for (int j_ = 0; j_ < 8; ++j_) pb_[j_] = __builtin_bit_cast(f32x4, __builtin_amdgcn_raw_buffer_load_b128(rB, boff, (64 * (t_) + 8 * j_) * LDB * 4, 0)); } while (0)
; #define XG_ISSUE_A(pa_, t_) do { _Pragma("unroll") for (int j_ = 0; j_ < 8; ++j_) pa_[j_] = __builtin_amdgcn_raw_buffer_load_b128(rA, aoff[j_], 128 * (t_), 0); } while (0)
; #define XG_STORE(pb_, pa_, bo_) do { _Pragma("unroll") for (int j_ = 0; j_ < 8; ++j_) *(LAS v2u*)(lds + (bo_) + bdst + 8 * j_ * XG_BP) = pk4(pb_[j_]); \
;             _Pragma("unroll") for (int j_ = 0; j_ < 8; ++j_) *(LAS v4u*)(lds + (bo_) + (arow + 32 * j_) * XG_AP + ach * 16) = pa_[j_]; } while (0)
; #define XG_STEP(t_, PBN, PAN, PBS, PAS) do { XG_ISSUE_A(PAN, (t_) + 2); { const int tb_ = ((t_) + 3 < NK) ? (t_) + 3 : NK - 1; XG_ISSUE_B(PBN, tb_); } \
;                 XG_STORE(PBS, PAS, (((t_) + 1) & 1) * XG_BUF); __syncthreads(); } while (0)
; template <bool UP>
; __device__ __forceinline__ void xgemm_unit(const Args& a, LAS unsigned char* lds, int e, int s, int cnt, int off_e, int rp, int tid, int lane, int wave) {
;     ...
;             __builtin_amdgcn_s_setprio(1);
;             int ras_ = 0; float rw_ = 0.f;
;             if (!UP) ras_ = LISTS[rp + ((tl < nrows) ? tl : nrows - 1)];
;             XG_ISSUE_A(pa0, 0); XG_ISSUE_B(pb0, 0); XG_ISSUE_A(pa1, 1); XG_ISSUE_B(pb1, 1); XG_ISSUE_B(pb2, 2);
;             XG_STORE(pb0, pa0, 0);
;             __syncthreads();
; #pragma unroll
;             for (int t = 0; t + 3 <= NK - 2; t += 3) {
;                 XG_STEP(t, pb0, pa2, pb1, pa1);
;                 if (!UP && t == 0) rw_ = RW[ras_];
;                 XG_STEP(t + 1, pb1, pa0, pb2, pa2);
;                 XG_STEP(t + 2, pb2, pa1, pb0, pa0);
	buffer_load_dwordx4 v[4:7], v14, s[8:11], s40 offen
	buffer_load_dwordx4 v[8:11], v18, s[8:11], s40 offen
	buffer_load_dwordx4 v[44:47], v22, s[8:11], s40 offen
	buffer_load_dwordx4 v[48:51], v26, s[8:11], s40 offen
	buffer_load_dwordx4 v[52:55], v30, s[8:11], s40 offen
	buffer_load_dwordx4 v[56:59], v34, s[8:11], s40 offen
	buffer_load_dwordx4 v[60:63], v38, s[8:11], s40 offen
	buffer_load_dwordx4 v[64:67], v42, s[8:11], s40 offen
	s_mov_b32 s0, 0x120000
	buffer_load_dwordx4 v[100:103], v2, s[12:15], s0 offen
	s_mov_b32 s0, 0x124000
	s_waitcnt vmcnt(32)
	v_cvt_pk_bf16_f32 v12, v180, v181
	v_cvt_pk_bf16_f32 v13, v182, v183
	buffer_load_dwordx4 v[104:107], v2, s[12:15], s0 offen
	s_mov_b32 s0, 0x128000
	ds_write_b64 v154, v[12:13] offset:58368
	s_waitcnt vmcnt(32)
	v_cvt_pk_bf16_f32 v12, v184, v185
	v_cvt_pk_bf16_f32 v13, v186, v187
	buffer_load_dwordx4 v[108:111], v2, s[12:15], s0 offen
	s_mov_b32 s0, 0x12c000
	ds_write_b64 v154, v[12:13] offset:60544
	s_waitcnt vmcnt(32)
	v_cvt_pk_bf16_f32 v12, v188, v189
	v_cvt_pk_bf16_f32 v13, v190, v191
	buffer_load_dwordx4 v[112:115], v2, s[12:15], s0 offen
	s_mov_b32 s0, 0x130000
	ds_write_b64 v154, v[12:13] offset:62720
	s_waitcnt vmcnt(32)
	v_cvt_pk_bf16_f32 v12, v192, v193
	v_cvt_pk_bf16_f32 v13, v194, v195
	buffer_load_dwordx4 v[116:119], v2, s[12:15], s0 offen
	s_mov_b32 s0, 0x134000
	ds_write_b64 v154, v[12:13] offset:64896
	s_waitcnt vmcnt(32)
	v_cvt_pk_bf16_f32 v12, v196, v197
	v_cvt_pk_bf16_f32 v13, v198, v199
	buffer_load_dwordx4 v[120:123], v2, s[12:15], s0 offen
	s_mov_b32 s0, 0x138000
	ds_write_b64 v155, v[12:13]
	s_waitcnt vmcnt(32)
	v_cvt_pk_bf16_f32 v12, v200, v201
	v_cvt_pk_bf16_f32 v13, v202, v203
	buffer_load_dwordx4 v[124:127], v2, s[12:15], s0 offen
	s_mov_b32 s0, 0x13c000
	ds_write_b64 v156, v[12:13]
	s_waitcnt vmcnt(32)
	v_cvt_pk_bf16_f32 v12, v204, v205
	v_cvt_pk_bf16_f32 v13, v206, v207
	buffer_load_dwordx4 v[176:179], v2, s[12:15], s0 offen
	ds_write_b64 v157, v[12:13]
	s_waitcnt vmcnt(32)
	v_cvt_pk_bf16_f32 v12, v208, v209
	v_cvt_pk_bf16_f32 v13, v210, v211
	ds_write_b64 v158, v[12:13]
	s_waitcnt vmcnt(31)
	ds_write_b128 v165, v[68:71] offset:58368
	s_waitcnt vmcnt(30)
	ds_write_b128 v165, v[72:75] offset:63488
	s_waitcnt vmcnt(29)
	ds_write_b128 v168, v[76:79] offset:58368
	s_waitcnt vmcnt(28)
	ds_write_b128 v166, v[80:83] offset:58368
	s_waitcnt vmcnt(27)
	ds_write_b128 v169, v[84:87] offset:58368
	s_waitcnt vmcnt(26)
	ds_write_b128 v169, v[88:91] offset:63488
	s_waitcnt vmcnt(25)
	ds_write_b128 v170, v[92:95] offset:63488
	s_waitcnt vmcnt(24)
	ds_write_b128 v167, v[96:99] offset:58368
	s_waitcnt lgkmcnt(0)
	s_barrier
	buffer_load_dwordx4 v[68:71], v14, s[8:11], s25 offen
	buffer_load_dwordx4 v[72:75], v18, s[8:11], s25 offen
	buffer_load_dwordx4 v[76:79], v22, s[8:11], s25 offen
	buffer_load_dwordx4 v[80:83], v26, s[8:11], s25 offen
	buffer_load_dwordx4 v[84:87], v30, s[8:11], s25 offen
	buffer_load_dwordx4 v[88:91], v34, s[8:11], s25 offen
	buffer_load_dwordx4 v[92:95], v38, s[8:11], s25 offen
	buffer_load_dwordx4 v[96:99], v42, s[8:11], s25 offen
	s_mov_b32 s0, 0x140000
	buffer_load_dwordx4 v[180:183], v2, s[12:15], s0 offen
	s_mov_b32 s0, 0x144000
	s_waitcnt vmcnt(32)
	v_cvt_pk_bf16_f32 v12, v212, v213
	v_cvt_pk_bf16_f32 v13, v214, v215
	buffer_load_dwordx4 v[184:187], v2, s[12:15], s0 offen
	s_mov_b32 s0, 0x148000
	ds_write_b64 v153, v[12:13] offset:40960
	s_waitcnt vmcnt(32)
	v_cvt_pk_bf16_f32 v12, v216, v217
	v_cvt_pk_bf16_f32 v13, v218, v219
	buffer_load_dwordx4 v[188:191], v2, s[12:15], s0 offen
	s_mov_b32 s0, 0x14c000
	ds_write_b64 v153, v[12:13] offset:43136
	s_waitcnt vmcnt(32)
	v_cvt_pk_bf16_f32 v12, v220, v221
	v_cvt_pk_bf16_f32 v13, v222, v223
	buffer_load_dwordx4 v[192:195], v2, s[12:15], s0 offen
	s_mov_b32 s0, 0x150000
	ds_write_b64 v153, v[12:13] offset:45312
	s_waitcnt vmcnt(32)
	v_cvt_pk_bf16_f32 v12, v224, v225
	v_cvt_pk_bf16_f32 v13, v226, v227
	buffer_load_dwordx4 v[196:199], v2, s[12:15], s0 offen
	s_mov_b32 s0, 0x154000
	ds_write_b64 v153, v[12:13] offset:47488
	s_waitcnt vmcnt(32)
	v_cvt_pk_bf16_f32 v12, v228, v229
	v_cvt_pk_bf16_f32 v13, v230, v231
	buffer_load_dwordx4 v[200:203], v2, s[12:15], s0 offen
	s_mov_b32 s0, 0x158000
	ds_write_b64 v153, v[12:13] offset:49664
	s_waitcnt vmcnt(32)
	v_cvt_pk_bf16_f32 v12, v232, v233
	v_cvt_pk_bf16_f32 v13, v234, v235
	buffer_load_dwordx4 v[204:207], v2, s[12:15], s0 offen
	s_mov_b32 s0, 0x15c000
	ds_write_b64 v153, v[12:13] offset:51840
	s_waitcnt vmcnt(32)
	v_cvt_pk_bf16_f32 v12, v236, v237
	v_cvt_pk_bf16_f32 v13, v238, v239
	buffer_load_dwordx4 v[208:211], v2, s[12:15], s0 offen
	ds_write_b64 v153, v[12:13] offset:54016
	s_waitcnt vmcnt(32)
	v_cvt_pk_bf16_f32 v12, v240, v241
	v_cvt_pk_bf16_f32 v13, v242, v243
	ds_write_b64 v153, v[12:13] offset:56192
	s_waitcnt vmcnt(31)
	ds_write_b128 v165, v[4:7]
	s_waitcnt vmcnt(30)
	ds_write_b128 v165, v[8:11] offset:5120
	s_waitcnt vmcnt(29)
	ds_write_b128 v165, v[44:47] offset:10240
	s_waitcnt vmcnt(28)
	ds_write_b128 v166, v[48:51]
	s_waitcnt vmcnt(27)
	ds_write_b128 v165, v[52:55] offset:20480
	s_waitcnt vmcnt(26)
	ds_write_b128 v165, v[56:59] offset:25600
	s_waitcnt vmcnt(25)
	ds_write_b128 v165, v[60:63] offset:30720
	s_waitcnt vmcnt(24)
	ds_write_b128 v167, v[64:67]
	s_waitcnt lgkmcnt(0)
	s_barrier
; #define XG_ISSUE_B(pb_, t_) do { _Pragma("unroll") for (int j_ = 0; j_ < 8; ++j_) pb_[j_] = __builtin_bit_cast(f32x4, __builtin_amdgcn_raw_buffer_load_b128(rB, boff, (64 * (t_) + 8 * j_) * LDB * 4, 0)); } while (0)
; #define XG_ISSUE_A(pa_, t_) do { _Pragma("unroll") for (int j_ = 0; j_ < 8; ++j_) pa_[j_] = __builtin_amdgcn_raw_buffer_load_b128(rA, aoff[j_], 128 * (t_), 0); } while (0)
; #define XG_STORE(pb_, pa_, bo_) do { _Pragma("unroll") for (int j_ = 0; j_ < 8; ++j_) *(LAS v2u*)(lds + (bo_) + bdst + 8 * j_ * XG_BP) = pk4(pb_[j_]); \
;             _Pragma("unroll") for (int j_ = 0; j_ < 8; ++j_) *(LAS v4u*)(lds + (bo_) + (arow + 32 * j_) * XG_AP + ach * 16) = pa_[j_]; } while (0)
; #define XG_STEP(t_, PBN, PAN, PBS, PAS) do { XG_ISSUE_A(PAN, (t_) + 2); { const int tb_ = ((t_) + 3 < NK) ? (t_) + 3 : NK - 1; XG_ISSUE_B(PBN, tb_); } \
;                 XG_STORE(PBS, PAS, (((t_) + 1) & 1) * XG_BUF); __syncthreads(); } while (0)
; template <bool UP>
; __device__ __forceinline__ void xgemm_unit(const Args& a, LAS unsigned char* lds, int e, int s, int cnt, int off_e, int rp, int tid, int lane, int wave) {
;     ...
;             __builtin_amdgcn_s_setprio(1);
;             int ras_ = 0; float rw_ = 0.f;
;             if (!UP) ras_ = LISTS[rp + ((tl < nrows) ? tl : nrows - 1)];
;             XG_ISSUE_A(pa0, 0); XG_ISSUE_B(pb0, 0); XG_ISSUE_A(pa1, 1); XG_ISSUE_B(pb1, 1); XG_ISSUE_B(pb2, 2);
;             XG_STORE(pb0, pa0, 0);
;             __syncthreads();
; #pragma unroll
;             for (int t = 0; t + 3 <= NK - 2; t += 3) {
;                 XG_STEP(t, pb0, pa2, pb1, pa1);
;                 if (!UP && t == 0) rw_ = RW[ras_];
;                 XG_STEP(t + 1, pb1, pa0, pb2, pa2);
;                 XG_STEP(t + 2, pb2, pa1, pb0, pa0);
	buffer_load_dwordx4 v[4:7], v14, s[8:11], s41 offen
	buffer_load_dwordx4 v[8:11], v18, s[8:11], s41 offen
	buffer_load_dwordx4 v[44:47], v22, s[8:11], s41 offen
	buffer_load_dwordx4 v[48:51], v26, s[8:11], s41 offen
	buffer_load_dwordx4 v[52:55], v30, s[8:11], s41 offen
	buffer_load_dwordx4 v[56:59], v34, s[8:11], s41 offen
	buffer_load_dwordx4 v[60:63], v38, s[8:11], s41 offen
	buffer_load_dwordx4 v[64:67], v42, s[8:11], s41 offen
	s_mov_b32 s0, 0x160000
	buffer_load_dwordx4 v[212:215], v2, s[12:15], s0 offen
	s_mov_b32 s0, 0x164000
	s_waitcnt vmcnt(32)
	v_cvt_pk_bf16_f32 v12, v100, v101
	v_cvt_pk_bf16_f32 v13, v102, v103
	buffer_load_dwordx4 v[216:219], v2, s[12:15], s0 offen
	s_mov_b32 s0, 0x168000
	ds_write_b64 v154, v[12:13] offset:58368
	s_waitcnt vmcnt(32)
	v_cvt_pk_bf16_f32 v12, v104, v105
	v_cvt_pk_bf16_f32 v13, v106, v107
	buffer_load_dwordx4 v[220:223], v2, s[12:15], s0 offen
	s_mov_b32 s0, 0x16c000
	ds_write_b64 v154, v[12:13] offset:60544
	s_waitcnt vmcnt(32)
	v_cvt_pk_bf16_f32 v12, v108, v109
	v_cvt_pk_bf16_f32 v13, v110, v111
	buffer_load_dwordx4 v[224:227], v2, s[12:15], s0 offen
	s_mov_b32 s0, 0x170000
	ds_write_b64 v154, v[12:13] offset:62720
	s_waitcnt vmcnt(32)
	v_cvt_pk_bf16_f32 v12, v112, v113
	v_cvt_pk_bf16_f32 v13, v114, v115
	buffer_load_dwordx4 v[228:231], v2, s[12:15], s0 offen
	s_mov_b32 s0, 0x174000
	ds_write_b64 v154, v[12:13] offset:64896
	s_waitcnt vmcnt(32)
	v_cvt_pk_bf16_f32 v12, v116, v117
	v_cvt_pk_bf16_f32 v13, v118, v119
	buffer_load_dwordx4 v[232:235], v2, s[12:15], s0 offen
	s_mov_b32 s0, 0x178000
	ds_write_b64 v155, v[12:13]
	s_waitcnt vmcnt(32)
	v_cvt_pk_bf16_f32 v12, v120, v121
	v_cvt_pk_bf16_f32 v13, v122, v123
	buffer_load_dwordx4 v[236:239], v2, s[12:15], s0 offen
	s_mov_b32 s0, 0x17c000
	ds_write_b64 v156, v[12:13]
	s_waitcnt vmcnt(32)
	v_cvt_pk_bf16_f32 v12, v124, v125
	v_cvt_pk_bf16_f32 v13, v126, v127
	buffer_load_dwordx4 v[240:243], v2, s[12:15], s0 offen
	ds_write_b64 v157, v[12:13]
	s_waitcnt vmcnt(32)
	v_cvt_pk_bf16_f32 v12, v176, v177
	v_cvt_pk_bf16_f32 v13, v178, v179
	ds_write_b64 v158, v[12:13]
	s_waitcnt vmcnt(31)
	ds_write_b128 v165, v[68:71] offset:58368
	s_waitcnt vmcnt(30)
	ds_write_b128 v165, v[72:75] offset:63488
	s_waitcnt vmcnt(29)
	ds_write_b128 v168, v[76:79] offset:58368
	s_waitcnt vmcnt(28)
	ds_write_b128 v166, v[80:83] offset:58368
	s_waitcnt vmcnt(27)
	ds_write_b128 v169, v[84:87] offset:58368
	s_waitcnt vmcnt(26)
	ds_write_b128 v169, v[88:91] offset:63488
	s_waitcnt vmcnt(25)
	ds_write_b128 v170, v[92:95] offset:63488
	s_waitcnt vmcnt(24)
	ds_write_b128 v167, v[96:99] offset:58368
	s_waitcnt lgkmcnt(0)
	s_barrier
	buffer_load_dwordx4 v[68:71], v14, s[8:11], s43 offen
	buffer_load_dwordx4 v[72:75], v18, s[8:11], s43 offen
	buffer_load_dwordx4 v[76:79], v22, s[8:11], s43 offen
	buffer_load_dwordx4 v[80:83], v26, s[8:11], s43 offen
	buffer_load_dwordx4 v[84:87], v30, s[8:11], s43 offen
	buffer_load_dwordx4 v[88:91], v34, s[8:11], s43 offen
	buffer_load_dwordx4 v[92:95], v38, s[8:11], s43 offen
	buffer_load_dwordx4 v[96:99], v42, s[8:11], s43 offen
	s_mov_b32 s0, 0x180000
	buffer_load_dwordx4 v[100:103], v2, s[12:15], s0 offen
	s_mov_b32 s0, 0x184000
	s_waitcnt vmcnt(32)
	v_cvt_pk_bf16_f32 v12, v180, v181
	v_cvt_pk_bf16_f32 v13, v182, v183
	buffer_load_dwordx4 v[104:107], v2, s[12:15], s0 offen
	s_mov_b32 s0, 0x188000
	ds_write_b64 v153, v[12:13] offset:40960
	s_waitcnt vmcnt(32)
	v_cvt_pk_bf16_f32 v12, v184, v185
	v_cvt_pk_bf16_f32 v13, v186, v187
	buffer_load_dwordx4 v[108:111], v2, s[12:15], s0 offen
	s_mov_b32 s0, 0x18c000
	ds_write_b64 v153, v[12:13] offset:43136
	s_waitcnt vmcnt(32)
	v_cvt_pk_bf16_f32 v12, v188, v189
	v_cvt_pk_bf16_f32 v13, v190, v191
	buffer_load_dwordx4 v[112:115], v2, s[12:15], s0 offen
	s_mov_b32 s0, 0x190000
	ds_write_b64 v153, v[12:13] offset:45312
	s_waitcnt vmcnt(32)
	v_cvt_pk_bf16_f32 v12, v192, v193
	v_cvt_pk_bf16_f32 v13, v194, v195
	buffer_load_dwordx4 v[116:119], v2, s[12:15], s0 offen
	s_mov_b32 s0, 0x194000
	ds_write_b64 v153, v[12:13] offset:47488
	s_waitcnt vmcnt(32)
	v_cvt_pk_bf16_f32 v12, v196, v197
	v_cvt_pk_bf16_f32 v13, v198, v199
	buffer_load_dwordx4 v[120:123], v2, s[12:15], s0 offen
	s_mov_b32 s0, 0x198000
	ds_write_b64 v153, v[12:13] offset:49664
	s_waitcnt vmcnt(32)
	v_cvt_pk_bf16_f32 v12, v200, v201
	v_cvt_pk_bf16_f32 v13, v202, v203
	buffer_load_dwordx4 v[124:127], v2, s[12:15], s0 offen
	s_mov_b32 s0, 0x19c000
	ds_write_b64 v153, v[12:13] offset:51840
	s_waitcnt vmcnt(32)
	v_cvt_pk_bf16_f32 v12, v204, v205
	v_cvt_pk_bf16_f32 v13, v206, v207
	buffer_load_dwordx4 v[176:179], v2, s[12:15], s0 offen
	ds_write_b64 v153, v[12:13] offset:54016
	s_waitcnt vmcnt(32)
	v_cvt_pk_bf16_f32 v12, v208, v209
	v_cvt_pk_bf16_f32 v13, v210, v211
	ds_write_b64 v153, v[12:13] offset:56192
	s_waitcnt vmcnt(31)
	ds_write_b128 v165, v[4:7]
	s_waitcnt vmcnt(30)
	ds_write_b128 v165, v[8:11] offset:5120
	s_waitcnt vmcnt(29)
	ds_write_b128 v165, v[44:47] offset:10240
	s_waitcnt vmcnt(28)
	ds_write_b128 v166, v[48:51]
	s_waitcnt vmcnt(27)
	ds_write_b128 v165, v[52:55] offset:20480
	s_waitcnt vmcnt(26)
	ds_write_b128 v165, v[56:59] offset:25600
	s_waitcnt vmcnt(25)
	ds_write_b128 v165, v[60:63] offset:30720
	s_waitcnt vmcnt(24)
	ds_write_b128 v167, v[64:67]
	s_waitcnt lgkmcnt(0)
	s_barrier
; #define XG_ISSUE_B(pb_, t_) do { _Pragma("unroll") for (int j_ = 0; j_ < 8; ++j_) pb_[j_] = __builtin_bit_cast(f32x4, __builtin_amdgcn_raw_buffer_load_b128(rB, boff, (64 * (t_) + 8 * j_) * LDB * 4, 0)); } while (0)
; #define XG_ISSUE_A(pa_, t_) do { _Pragma("unroll") for (int j_ = 0; j_ < 8; ++j_) pa_[j_] = __builtin_amdgcn_raw_buffer_load_b128(rA, aoff[j_], 128 * (t_), 0); } while (0)
; #define XG_STORE(pb_, pa_, bo_) do { _Pragma("unroll") for (int j_ = 0; j_ < 8; ++j_) *(LAS v2u*)(lds + (bo_) + bdst + 8 * j_ * XG_BP) = pk4(pb_[j_]); \
;             _Pragma("unroll") for (int j_ = 0; j_ < 8; ++j_) *(LAS v4u*)(lds + (bo_) + (arow + 32 * j_) * XG_AP + ach * 16) = pa_[j_]; } while (0)
; #define XG_STEP(t_, PBN, PAN, PBS, PAS) do { XG_ISSUE_A(PAN, (t_) + 2); { const int tb_ = ((t_) + 3 < NK) ? (t_) + 3 : NK - 1; XG_ISSUE_B(PBN, tb_); } \
;                 XG_STORE(PBS, PAS, (((t_) + 1) & 1) * XG_BUF); __syncthreads(); } while (0)
; template <bool UP>
; __device__ __forceinline__ void xgemm_unit(const Args& a, LAS unsigned char* lds, int e, int s, int cnt, int off_e, int rp, int tid, int lane, int wave) {
;     ...
;             __builtin_amdgcn_s_setprio(1);
;             int ras_ = 0; float rw_ = 0.f;
;             if (!UP) ras_ = LISTS[rp + ((tl < nrows) ? tl : nrows - 1)];
;             XG_ISSUE_A(pa0, 0); XG_ISSUE_B(pb0, 0); XG_ISSUE_A(pa1, 1); XG_ISSUE_B(pb1, 1); XG_ISSUE_B(pb2, 2);
;             XG_STORE(pb0, pa0, 0);
;             __syncthreads();
; #pragma unroll
;             for (int t = 0; t + 3 <= NK - 2; t += 3) {
;                 XG_STEP(t, pb0, pa2, pb1, pa1);
;                 if (!UP && t == 0) rw_ = RW[ras_];
;                 XG_STEP(t + 1, pb1, pa0, pb2, pa2);
;                 XG_STEP(t + 2, pb2, pa1, pb0, pa0);
	buffer_load_dwordx4 v[4:7], v14, s[8:11], s44 offen
	buffer_load_dwordx4 v[8:11], v18, s[8:11], s44 offen
	buffer_load_dwordx4 v[44:47], v22, s[8:11], s44 offen
	buffer_load_dwordx4 v[48:51], v26, s[8:11], s44 offen
	buffer_load_dwordx4 v[52:55], v30, s[8:11], s44 offen
	buffer_load_dwordx4 v[56:59], v34, s[8:11], s44 offen
	buffer_load_dwordx4 v[60:63], v38, s[8:11], s44 offen
	buffer_load_dwordx4 v[64:67], v42, s[8:11], s44 offen
	s_mov_b32 s0, 0x1a0000
	buffer_load_dwordx4 v[180:183], v2, s[12:15], s0 offen
	s_mov_b32 s0, 0x1a4000
	s_waitcnt vmcnt(32)
	v_cvt_pk_bf16_f32 v12, v212, v213
	v_cvt_pk_bf16_f32 v13, v214, v215
	buffer_load_dwordx4 v[184:187], v2, s[12:15], s0 offen
	s_mov_b32 s0, 0x1a8000
	ds_write_b64 v154, v[12:13] offset:58368
	s_waitcnt vmcnt(32)
	v_cvt_pk_bf16_f32 v12, v216, v217
	v_cvt_pk_bf16_f32 v13, v218, v219
	buffer_load_dwordx4 v[188:191], v2, s[12:15], s0 offen
	s_mov_b32 s0, 0x1ac000
	ds_write_b64 v154, v[12:13] offset:60544
	s_waitcnt vmcnt(32)
	v_cvt_pk_bf16_f32 v12, v220, v221
	v_cvt_pk_bf16_f32 v13, v222, v223
	buffer_load_dwordx4 v[192:195], v2, s[12:15], s0 offen
	s_mov_b32 s0, 0x1b0000
	ds_write_b64 v154, v[12:13] offset:62720
	s_waitcnt vmcnt(32)
	v_cvt_pk_bf16_f32 v12, v224, v225
	v_cvt_pk_bf16_f32 v13, v226, v227
	buffer_load_dwordx4 v[196:199], v2, s[12:15], s0 offen
	s_mov_b32 s0, 0x1b4000
	ds_write_b64 v154, v[12:13] offset:64896
	s_waitcnt vmcnt(32)
	v_cvt_pk_bf16_f32 v12, v228, v229
	v_cvt_pk_bf16_f32 v13, v230, v231
	buffer_load_dwordx4 v[200:203], v2, s[12:15], s0 offen
	s_mov_b32 s0, 0x1b8000
	ds_write_b64 v155, v[12:13]
	s_waitcnt vmcnt(32)
	v_cvt_pk_bf16_f32 v12, v232, v233
	v_cvt_pk_bf16_f32 v13, v234, v235
	buffer_load_dwordx4 v[204:207], v2, s[12:15], s0 offen
	s_mov_b32 s0, 0x1bc000
	ds_write_b64 v156, v[12:13]
	s_waitcnt vmcnt(32)
	v_cvt_pk_bf16_f32 v12, v236, v237
	v_cvt_pk_bf16_f32 v13, v238, v239
	buffer_load_dwordx4 v[208:211], v2, s[12:15], s0 offen
	ds_write_b64 v157, v[12:13]
	s_waitcnt vmcnt(32)
	v_cvt_pk_bf16_f32 v12, v240, v241
	v_cvt_pk_bf16_f32 v13, v242, v243
	ds_write_b64 v158, v[12:13]
	s_waitcnt vmcnt(31)
	ds_write_b128 v165, v[68:71] offset:58368
	s_waitcnt vmcnt(30)
	ds_write_b128 v165, v[72:75] offset:63488
	s_waitcnt vmcnt(29)
	ds_write_b128 v168, v[76:79] offset:58368
	s_waitcnt vmcnt(28)
	ds_write_b128 v166, v[80:83] offset:58368
	s_waitcnt vmcnt(27)
	ds_write_b128 v169, v[84:87] offset:58368
	s_waitcnt vmcnt(26)
	ds_write_b128 v169, v[88:91] offset:63488
	s_waitcnt vmcnt(25)
	ds_write_b128 v170, v[92:95] offset:63488
	s_waitcnt vmcnt(24)
	ds_write_b128 v167, v[96:99] offset:58368
	s_waitcnt lgkmcnt(0)
	s_barrier
	buffer_load_dwordx4 v[68:71], v14, s[8:11], s45 offen
	buffer_load_dwordx4 v[72:75], v18, s[8:11], s45 offen
	buffer_load_dwordx4 v[76:79], v22, s[8:11], s45 offen
	buffer_load_dwordx4 v[80:83], v26, s[8:11], s45 offen
	buffer_load_dwordx4 v[84:87], v30, s[8:11], s45 offen
	buffer_load_dwordx4 v[88:91], v34, s[8:11], s45 offen
	buffer_load_dwordx4 v[92:95], v38, s[8:11], s45 offen
	buffer_load_dwordx4 v[96:99], v42, s[8:11], s45 offen
	s_mov_b32 s0, 0x1c0000
	buffer_load_dwordx4 v[212:215], v2, s[12:15], s0 offen
	s_mov_b32 s0, 0x1c4000
	s_waitcnt vmcnt(32)
	v_cvt_pk_bf16_f32 v12, v100, v101
	v_cvt_pk_bf16_f32 v13, v102, v103
	buffer_load_dwordx4 v[216:219], v2, s[12:15], s0 offen
	s_mov_b32 s0, 0x1c8000
	ds_write_b64 v153, v[12:13] offset:40960
	s_waitcnt vmcnt(32)
	v_cvt_pk_bf16_f32 v12, v104, v105
	v_cvt_pk_bf16_f32 v13, v106, v107
	buffer_load_dwordx4 v[220:223], v2, s[12:15], s0 offen
	s_mov_b32 s0, 0x1cc000
	ds_write_b64 v153, v[12:13] offset:43136
	s_waitcnt vmcnt(32)
	v_cvt_pk_bf16_f32 v12, v108, v109
	v_cvt_pk_bf16_f32 v13, v110, v111
	buffer_load_dwordx4 v[224:227], v2, s[12:15], s0 offen
	s_mov_b32 s0, 0x1d0000
	ds_write_b64 v153, v[12:13] offset:45312
	s_waitcnt vmcnt(32)
	v_cvt_pk_bf16_f32 v12, v112, v113
	v_cvt_pk_bf16_f32 v13, v114, v115
	buffer_load_dwordx4 v[228:231], v2, s[12:15], s0 offen
	s_mov_b32 s0, 0x1d4000
	ds_write_b64 v153, v[12:13] offset:47488
	s_waitcnt vmcnt(32)
	v_cvt_pk_bf16_f32 v12, v116, v117
	v_cvt_pk_bf16_f32 v13, v118, v119
	buffer_load_dwordx4 v[232:235], v2, s[12:15], s0 offen
	s_mov_b32 s0, 0x1d8000
	ds_write_b64 v153, v[12:13] offset:49664
	s_waitcnt vmcnt(32)
	v_cvt_pk_bf16_f32 v12, v120, v121
	v_cvt_pk_bf16_f32 v13, v122, v123
	buffer_load_dwordx4 v[236:239], v2, s[12:15], s0 offen
	s_mov_b32 s0, 0x1dc000
	ds_write_b64 v153, v[12:13] offset:51840
	s_waitcnt vmcnt(32)
	v_cvt_pk_bf16_f32 v12, v124, v125
	v_cvt_pk_bf16_f32 v13, v126, v127
	buffer_load_dwordx4 v[240:243], v2, s[12:15], s0 offen
	ds_write_b64 v153, v[12:13] offset:54016
	s_waitcnt vmcnt(32)
	v_cvt_pk_bf16_f32 v12, v176, v177
	v_cvt_pk_bf16_f32 v13, v178, v179
	ds_write_b64 v153, v[12:13] offset:56192
	s_waitcnt vmcnt(31)
	ds_write_b128 v165, v[4:7]
	s_waitcnt vmcnt(30)
	ds_write_b128 v165, v[8:11] offset:5120
	s_waitcnt vmcnt(29)
	ds_write_b128 v165, v[44:47] offset:10240
	s_waitcnt vmcnt(28)
	ds_write_b128 v166, v[48:51]
	s_waitcnt vmcnt(27)
	ds_write_b128 v165, v[52:55] offset:20480
	s_waitcnt vmcnt(26)
	ds_write_b128 v165, v[56:59] offset:25600
	s_waitcnt vmcnt(25)
	ds_write_b128 v165, v[60:63] offset:30720
	s_waitcnt vmcnt(24)
	ds_write_b128 v167, v[64:67]
	s_waitcnt lgkmcnt(0)
	s_barrier
; #define XG_ISSUE_B(pb_, t_) do { _Pragma("unroll") for (int j_ = 0; j_ < 8; ++j_) pb_[j_] = __builtin_bit_cast(f32x4, __builtin_amdgcn_raw_buffer_load_b128(rB, boff, (64 * (t_) + 8 * j_) * LDB * 4, 0)); } while (0)
; #define XG_ISSUE_A(pa_, t_) do { _Pragma("unroll") for (int j_ = 0; j_ < 8; ++j_) pa_[j_] = __builtin_amdgcn_raw_buffer_load_b128(rA, aoff[j_], 128 * (t_), 0); } while (0)
; #define XG_STORE(pb_, pa_, bo_) do { _Pragma("unroll") for (int j_ = 0; j_ < 8; ++j_) *(LAS v2u*)(lds + (bo_) + bdst + 8 * j_ * XG_BP) = pk4(pb_[j_]); \
;             _Pragma("unroll") for (int j_ = 0; j_ < 8; ++j_) *(LAS v4u*)(lds + (bo_) + (arow + 32 * j_) * XG_AP + ach * 16) = pa_[j_]; } while (0)
; #define XG_STEP(t_, PBN, PAN, PBS, PAS) do { XG_ISSUE_A(PAN, (t_) + 2); { const int tb_ = ((t_) + 3 < NK) ? (t_) + 3 : NK - 1; XG_ISSUE_B(PBN, tb_); } \
;                 XG_STORE(PBS, PAS, (((t_) + 1) & 1) * XG_BUF); __syncthreads(); } while (0)
; template <bool UP>
; __device__ __forceinline__ void xgemm_unit(const Args& a, LAS unsigned char* lds, int e, int s, int cnt, int off_e, int rp, int tid, int lane, int wave) {
;     ...
;             __builtin_amdgcn_s_setprio(1);
;             int ras_ = 0; float rw_ = 0.f;
;             if (!UP) ras_ = LISTS[rp + ((tl < nrows) ? tl : nrows - 1)];
;             XG_ISSUE_A(pa0, 0); XG_ISSUE_B(pb0, 0); XG_ISSUE_A(pa1, 1); XG_ISSUE_B(pb1, 1); XG_ISSUE_B(pb2, 2);
;             XG_STORE(pb0, pa0, 0);
;             __syncthreads();
; #pragma unroll
;             for (int t = 0; t + 3 <= NK - 2; t += 3) {
;                 XG_STEP(t, pb0, pa2, pb1, pa1);
;                 if (!UP && t == 0) rw_ = RW[ras_];
;                 XG_STEP(t + 1, pb1, pa0, pb2, pa2);
;                 XG_STEP(t + 2, pb2, pa1, pb0, pa0);
	buffer_load_dwordx4 v[4:7], v14, s[8:11], s46 offen
	buffer_load_dwordx4 v[8:11], v18, s[8:11], s46 offen
	buffer_load_dwordx4 v[44:47], v22, s[8:11], s46 offen
	buffer_load_dwordx4 v[48:51], v26, s[8:11], s46 offen
	buffer_load_dwordx4 v[52:55], v30, s[8:11], s46 offen
	buffer_load_dwordx4 v[56:59], v34, s[8:11], s46 offen
	buffer_load_dwordx4 v[60:63], v38, s[8:11], s46 offen
	buffer_load_dwordx4 v[64:67], v42, s[8:11], s46 offen
	s_mov_b32 s0, 0x1e0000
	buffer_load_dwordx4 v[100:103], v2, s[12:15], s0 offen
	s_mov_b32 s0, 0x1e4000
	s_waitcnt vmcnt(32)
	v_cvt_pk_bf16_f32 v12, v180, v181
	v_cvt_pk_bf16_f32 v13, v182, v183
	buffer_load_dwordx4 v[104:107], v2, s[12:15], s0 offen
	s_mov_b32 s0, 0x1e8000
	ds_write_b64 v154, v[12:13] offset:58368
	s_waitcnt vmcnt(32)
	v_cvt_pk_bf16_f32 v12, v184, v185
	v_cvt_pk_bf16_f32 v13, v186, v187
	buffer_load_dwordx4 v[108:111], v2, s[12:15], s0 offen
	s_mov_b32 s0, 0x1ec000
	ds_write_b64 v154, v[12:13] offset:60544
	s_waitcnt vmcnt(32)
	v_cvt_pk_bf16_f32 v12, v188, v189
	v_cvt_pk_bf16_f32 v13, v190, v191
	buffer_load_dwordx4 v[112:115], v2, s[12:15], s0 offen
	s_mov_b32 s0, 0x1f0000
	ds_write_b64 v154, v[12:13] offset:62720
	s_waitcnt vmcnt(32)
	v_cvt_pk_bf16_f32 v12, v192, v193
	v_cvt_pk_bf16_f32 v13, v194, v195
	buffer_load_dwordx4 v[116:119], v2, s[12:15], s0 offen
	s_mov_b32 s0, 0x1f4000
	ds_write_b64 v154, v[12:13] offset:64896
	s_waitcnt vmcnt(32)
	v_cvt_pk_bf16_f32 v12, v196, v197
	v_cvt_pk_bf16_f32 v13, v198, v199
	buffer_load_dwordx4 v[120:123], v2, s[12:15], s0 offen
	s_mov_b32 s0, 0x1f8000
	ds_write_b64 v155, v[12:13]
	s_waitcnt vmcnt(32)
	v_cvt_pk_bf16_f32 v12, v200, v201
	v_cvt_pk_bf16_f32 v13, v202, v203
	buffer_load_dwordx4 v[124:127], v2, s[12:15], s0 offen
	s_mov_b32 s0, 0x1fc000
	ds_write_b64 v156, v[12:13]
	s_waitcnt vmcnt(32)
	v_cvt_pk_bf16_f32 v12, v204, v205
	v_cvt_pk_bf16_f32 v13, v206, v207
	buffer_load_dwordx4 v[176:179], v2, s[12:15], s0 offen
	ds_write_b64 v157, v[12:13]
	s_waitcnt vmcnt(32)
	v_cvt_pk_bf16_f32 v12, v208, v209
	v_cvt_pk_bf16_f32 v13, v210, v211
	ds_write_b64 v158, v[12:13]
	s_waitcnt vmcnt(31)
	ds_write_b128 v165, v[68:71] offset:58368
	s_waitcnt vmcnt(30)
	ds_write_b128 v165, v[72:75] offset:63488
	s_waitcnt vmcnt(29)
	ds_write_b128 v168, v[76:79] offset:58368
	s_waitcnt vmcnt(28)
	ds_write_b128 v166, v[80:83] offset:58368
	s_waitcnt vmcnt(27)
	ds_write_b128 v169, v[84:87] offset:58368
	s_waitcnt vmcnt(26)
	ds_write_b128 v169, v[88:91] offset:63488
	s_waitcnt vmcnt(25)
	ds_write_b128 v170, v[92:95] offset:63488
	s_waitcnt vmcnt(24)
	ds_write_b128 v167, v[96:99] offset:58368
	s_waitcnt lgkmcnt(0)
	s_barrier
	buffer_load_dwordx4 v[68:71], v14, s[8:11], s47 offen
	buffer_load_dwordx4 v[72:75], v18, s[8:11], s47 offen
	buffer_load_dwordx4 v[76:79], v22, s[8:11], s47 offen
	buffer_load_dwordx4 v[80:83], v26, s[8:11], s47 offen
	buffer_load_dwordx4 v[84:87], v30, s[8:11], s47 offen
	buffer_load_dwordx4 v[88:91], v34, s[8:11], s47 offen
	buffer_load_dwordx4 v[92:95], v38, s[8:11], s47 offen
	buffer_load_dwordx4 v[96:99], v42, s[8:11], s47 offen
	s_mov_b32 s0, 0x200000
	buffer_load_dwordx4 v[180:183], v2, s[12:15], s0 offen
	s_mov_b32 s0, 0x204000
	s_waitcnt vmcnt(32)
	v_cvt_pk_bf16_f32 v12, v212, v213
	v_cvt_pk_bf16_f32 v13, v214, v215
	buffer_load_dwordx4 v[184:187], v2, s[12:15], s0 offen
	s_mov_b32 s0, 0x208000
	ds_write_b64 v153, v[12:13] offset:40960
	s_waitcnt vmcnt(32)
	v_cvt_pk_bf16_f32 v12, v216, v217
	v_cvt_pk_bf16_f32 v13, v218, v219
	buffer_load_dwordx4 v[188:191], v2, s[12:15], s0 offen
	s_mov_b32 s0, 0x20c000
	ds_write_b64 v153, v[12:13] offset:43136
	s_waitcnt vmcnt(32)
	v_cvt_pk_bf16_f32 v12, v220, v221
	v_cvt_pk_bf16_f32 v13, v222, v223
	buffer_load_dwordx4 v[192:195], v2, s[12:15], s0 offen
	s_mov_b32 s0, 0x210000
	ds_write_b64 v153, v[12:13] offset:45312
	s_waitcnt vmcnt(32)
	v_cvt_pk_bf16_f32 v12, v224, v225
	v_cvt_pk_bf16_f32 v13, v226, v227
	buffer_load_dwordx4 v[196:199], v2, s[12:15], s0 offen
	s_mov_b32 s0, 0x214000
	ds_write_b64 v153, v[12:13] offset:47488
	s_waitcnt vmcnt(32)
	v_cvt_pk_bf16_f32 v12, v228, v229
	v_cvt_pk_bf16_f32 v13, v230, v231
	buffer_load_dwordx4 v[200:203], v2, s[12:15], s0 offen
	s_mov_b32 s0, 0x218000
	ds_write_b64 v153, v[12:13] offset:49664
	s_waitcnt vmcnt(32)
	v_cvt_pk_bf16_f32 v12, v232, v233
	v_cvt_pk_bf16_f32 v13, v234, v235
	buffer_load_dwordx4 v[204:207], v2, s[12:15], s0 offen
	s_mov_b32 s0, 0x21c000
	ds_write_b64 v153, v[12:13] offset:51840
	s_waitcnt vmcnt(32)
	v_cvt_pk_bf16_f32 v12, v236, v237
	v_cvt_pk_bf16_f32 v13, v238, v239
	buffer_load_dwordx4 v[208:211], v2, s[12:15], s0 offen
	ds_write_b64 v153, v[12:13] offset:54016
	s_waitcnt vmcnt(32)
	v_cvt_pk_bf16_f32 v12, v240, v241
	v_cvt_pk_bf16_f32 v13, v242, v243
	ds_write_b64 v153, v[12:13] offset:56192
	s_waitcnt vmcnt(31)
	ds_write_b128 v165, v[4:7]
	s_waitcnt vmcnt(30)
	ds_write_b128 v165, v[8:11] offset:5120
	s_waitcnt vmcnt(29)
	ds_write_b128 v165, v[44:47] offset:10240
	s_waitcnt vmcnt(28)
	ds_write_b128 v166, v[48:51]
	s_waitcnt vmcnt(27)
	ds_write_b128 v165, v[52:55] offset:20480
	s_waitcnt vmcnt(26)
	ds_write_b128 v165, v[56:59] offset:25600
	s_waitcnt vmcnt(25)
	ds_write_b128 v165, v[60:63] offset:30720
	s_waitcnt vmcnt(24)
	ds_write_b128 v167, v[64:67]
	s_waitcnt lgkmcnt(0)
	s_barrier
; #define XG_ISSUE_B(pb_, t_) do { _Pragma("unroll") for (int j_ = 0; j_ < 8; ++j_) pb_[j_] = __builtin_bit_cast(f32x4, __builtin_amdgcn_raw_buffer_load_b128(rB, boff, (64 * (t_) + 8 * j_) * LDB * 4, 0)); } while (0)
; #define XG_ISSUE_A(pa_, t_) do { _Pragma("unroll") for (int j_ = 0; j_ < 8; ++j_) pa_[j_] = __builtin_amdgcn_raw_buffer_load_b128(rA, aoff[j_], 128 * (t_), 0); } while (0)
; #define XG_STORE(pb_, pa_, bo_) do { _Pragma("unroll") for (int j_ = 0; j_ < 8; ++j_) *(LAS v2u*)(lds + (bo_) + bdst + 8 * j_ * XG_BP) = pk4(pb_[j_]); \
;             _Pragma("unroll") for (int j_ = 0; j_ < 8; ++j_) *(LAS v4u*)(lds + (bo_) + (arow + 32 * j_) * XG_AP + ach * 16) = pa_[j_]; } while (0)
; #define XG_STEP(t_, PBN, PAN, PBS, PAS) do { XG_ISSUE_A(PAN, (t_) + 2); { const int tb_ = ((t_) + 3 < NK) ? (t_) + 3 : NK - 1; XG_ISSUE_B(PBN, tb_); } \
;                 XG_STORE(PBS, PAS, (((t_) + 1) & 1) * XG_BUF); __syncthreads(); } while (0)
; template <bool UP>
; __device__ __forceinline__ void xgemm_unit(const Args& a, LAS unsigned char* lds, int e, int s, int cnt, int off_e, int rp, int tid, int lane, int wave) {
;     ...
;             __builtin_amdgcn_s_setprio(1);
;             int ras_ = 0; float rw_ = 0.f;
;             if (!UP) ras_ = LISTS[rp + ((tl < nrows) ? tl : nrows - 1)];
;             XG_ISSUE_A(pa0, 0); XG_ISSUE_B(pb0, 0); XG_ISSUE_A(pa1, 1); XG_ISSUE_B(pb1, 1); XG_ISSUE_B(pb2, 2);
;             XG_STORE(pb0, pa0, 0);
;             __syncthreads();
; #pragma unroll
;             for (int t = 0; t + 3 <= NK - 2; t += 3) {
;                 XG_STEP(t, pb0, pa2, pb1, pa1);
;                 if (!UP && t == 0) rw_ = RW[ras_];
;                 XG_STEP(t + 1, pb1, pa0, pb2, pa2);
;                 XG_STEP(t + 2, pb2, pa1, pb0, pa0);
	buffer_load_dwordx4 v[4:7], v14, s[8:11], s48 offen
	buffer_load_dwordx4 v[8:11], v18, s[8:11], s48 offen
	buffer_load_dwordx4 v[44:47], v22, s[8:11], s48 offen
	buffer_load_dwordx4 v[48:51], v26, s[8:11], s48 offen
	buffer_load_dwordx4 v[52:55], v30, s[8:11], s48 offen
	buffer_load_dwordx4 v[56:59], v34, s[8:11], s48 offen
	buffer_load_dwordx4 v[60:63], v38, s[8:11], s48 offen
	buffer_load_dwordx4 v[64:67], v42, s[8:11], s48 offen
	s_mov_b32 s0, 0x220000
	buffer_load_dwordx4 v[212:215], v2, s[12:15], s0 offen
	s_mov_b32 s0, 0x224000
	s_waitcnt vmcnt(32)
	v_cvt_pk_bf16_f32 v12, v100, v101
	v_cvt_pk_bf16_f32 v13, v102, v103
	buffer_load_dwordx4 v[216:219], v2, s[12:15], s0 offen
	s_mov_b32 s0, 0x228000
	ds_write_b64 v154, v[12:13] offset:58368
	s_waitcnt vmcnt(32)
	v_cvt_pk_bf16_f32 v12, v104, v105
	v_cvt_pk_bf16_f32 v13, v106, v107
	buffer_load_dwordx4 v[220:223], v2, s[12:15], s0 offen
	s_mov_b32 s0, 0x22c000
	ds_write_b64 v154, v[12:13] offset:60544
	s_waitcnt vmcnt(32)
	v_cvt_pk_bf16_f32 v12, v108, v109
	v_cvt_pk_bf16_f32 v13, v110, v111
	buffer_load_dwordx4 v[224:227], v2, s[12:15], s0 offen
	s_mov_b32 s0, 0x230000
	ds_write_b64 v154, v[12:13] offset:62720
	s_waitcnt vmcnt(32)
	v_cvt_pk_bf16_f32 v12, v112, v113
	v_cvt_pk_bf16_f32 v13, v114, v115
	buffer_load_dwordx4 v[228:231], v2, s[12:15], s0 offen
	s_mov_b32 s0, 0x234000
	ds_write_b64 v154, v[12:13] offset:64896
	s_waitcnt vmcnt(32)
	v_cvt_pk_bf16_f32 v12, v116, v117
	v_cvt_pk_bf16_f32 v13, v118, v119
	buffer_load_dwordx4 v[232:235], v2, s[12:15], s0 offen
	s_mov_b32 s0, 0x238000
	ds_write_b64 v155, v[12:13]
	s_waitcnt vmcnt(32)
	v_cvt_pk_bf16_f32 v12, v120, v121
	v_cvt_pk_bf16_f32 v13, v122, v123
	buffer_load_dwordx4 v[236:239], v2, s[12:15], s0 offen
	s_mov_b32 s0, 0x23c000
	ds_write_b64 v156, v[12:13]
	s_waitcnt vmcnt(32)
	v_cvt_pk_bf16_f32 v12, v124, v125
	v_cvt_pk_bf16_f32 v13, v126, v127
	buffer_load_dwordx4 v[240:243], v2, s[12:15], s0 offen
	ds_write_b64 v157, v[12:13]
	s_waitcnt vmcnt(32)
	v_cvt_pk_bf16_f32 v12, v176, v177
	v_cvt_pk_bf16_f32 v13, v178, v179
	ds_write_b64 v158, v[12:13]
	s_waitcnt vmcnt(31)
	ds_write_b128 v165, v[68:71] offset:58368
	s_waitcnt vmcnt(30)
	ds_write_b128 v165, v[72:75] offset:63488
	s_waitcnt vmcnt(29)
	ds_write_b128 v168, v[76:79] offset:58368
	s_waitcnt vmcnt(28)
	ds_write_b128 v166, v[80:83] offset:58368
	s_waitcnt vmcnt(27)
	ds_write_b128 v169, v[84:87] offset:58368
	s_waitcnt vmcnt(26)
	ds_write_b128 v169, v[88:91] offset:63488
	s_waitcnt vmcnt(25)
	ds_write_b128 v170, v[92:95] offset:63488
	s_waitcnt vmcnt(24)
	ds_write_b128 v167, v[96:99] offset:58368
	s_waitcnt lgkmcnt(0)
	s_barrier
	buffer_load_dwordx4 v[68:71], v14, s[8:11], s49 offen
	buffer_load_dwordx4 v[72:75], v18, s[8:11], s49 offen
	buffer_load_dwordx4 v[76:79], v22, s[8:11], s49 offen
	buffer_load_dwordx4 v[80:83], v26, s[8:11], s49 offen
	buffer_load_dwordx4 v[84:87], v30, s[8:11], s49 offen
	buffer_load_dwordx4 v[88:91], v34, s[8:11], s49 offen
	buffer_load_dwordx4 v[92:95], v38, s[8:11], s49 offen
	buffer_load_dwordx4 v[96:99], v42, s[8:11], s49 offen
	s_mov_b32 s0, 0x240000
	buffer_load_dwordx4 v[100:103], v2, s[12:15], s0 offen
	s_mov_b32 s0, 0x244000
	s_waitcnt vmcnt(32)
	v_cvt_pk_bf16_f32 v12, v180, v181
	v_cvt_pk_bf16_f32 v13, v182, v183
	buffer_load_dwordx4 v[104:107], v2, s[12:15], s0 offen
	s_mov_b32 s0, 0x248000
	ds_write_b64 v153, v[12:13] offset:40960
	s_waitcnt vmcnt(32)
	v_cvt_pk_bf16_f32 v12, v184, v185
	v_cvt_pk_bf16_f32 v13, v186, v187
	buffer_load_dwordx4 v[108:111], v2, s[12:15], s0 offen
	s_mov_b32 s0, 0x24c000
	ds_write_b64 v153, v[12:13] offset:43136
	s_waitcnt vmcnt(32)
	v_cvt_pk_bf16_f32 v12, v188, v189
	v_cvt_pk_bf16_f32 v13, v190, v191
	buffer_load_dwordx4 v[112:115], v2, s[12:15], s0 offen
	s_mov_b32 s0, 0x250000
	ds_write_b64 v153, v[12:13] offset:45312
	s_waitcnt vmcnt(32)
	v_cvt_pk_bf16_f32 v12, v192, v193
	v_cvt_pk_bf16_f32 v13, v194, v195
	buffer_load_dwordx4 v[116:119], v2, s[12:15], s0 offen
	s_mov_b32 s0, 0x254000
	ds_write_b64 v153, v[12:13] offset:47488
	s_waitcnt vmcnt(32)
	v_cvt_pk_bf16_f32 v12, v196, v197
	v_cvt_pk_bf16_f32 v13, v198, v199
	buffer_load_dwordx4 v[120:123], v2, s[12:15], s0 offen
	s_mov_b32 s0, 0x258000
	ds_write_b64 v153, v[12:13] offset:49664
	s_waitcnt vmcnt(32)
	v_cvt_pk_bf16_f32 v12, v200, v201
	v_cvt_pk_bf16_f32 v13, v202, v203
	buffer_load_dwordx4 v[124:127], v2, s[12:15], s0 offen
	s_mov_b32 s0, 0x25c000
	ds_write_b64 v153, v[12:13] offset:51840
	s_waitcnt vmcnt(32)
	v_cvt_pk_bf16_f32 v12, v204, v205
	v_cvt_pk_bf16_f32 v13, v206, v207
	buffer_load_dwordx4 v[176:179], v2, s[12:15], s0 offen
	ds_write_b64 v153, v[12:13] offset:54016
	s_waitcnt vmcnt(32)
	v_cvt_pk_bf16_f32 v12, v208, v209
	v_cvt_pk_bf16_f32 v13, v210, v211
	ds_write_b64 v153, v[12:13] offset:56192
	s_waitcnt vmcnt(31)
	ds_write_b128 v165, v[4:7]
	s_waitcnt vmcnt(30)
	ds_write_b128 v165, v[8:11] offset:5120
	s_waitcnt vmcnt(29)
	ds_write_b128 v165, v[44:47] offset:10240
	s_waitcnt vmcnt(28)
	ds_write_b128 v166, v[48:51]
	s_waitcnt vmcnt(27)
	ds_write_b128 v165, v[52:55] offset:20480
	s_waitcnt vmcnt(26)
	ds_write_b128 v165, v[56:59] offset:25600
	s_waitcnt vmcnt(25)
	ds_write_b128 v165, v[60:63] offset:30720
	s_waitcnt vmcnt(24)
	ds_write_b128 v167, v[64:67]
	s_waitcnt lgkmcnt(0)
	s_barrier
; #define XG_ISSUE_B(pb_, t_) do { _Pragma("unroll") for (int j_ = 0; j_ < 8; ++j_) pb_[j_] = __builtin_bit_cast(f32x4, __builtin_amdgcn_raw_buffer_load_b128(rB, boff, (64 * (t_) + 8 * j_) * LDB * 4, 0)); } while (0)
; #define XG_ISSUE_A(pa_, t_) do { _Pragma("unroll") for (int j_ = 0; j_ < 8; ++j_) pa_[j_] = __builtin_amdgcn_raw_buffer_load_b128(rA, aoff[j_], 128 * (t_), 0); } while (0)
; #define XG_STORE(pb_, pa_, bo_) do { _Pragma("unroll") for (int j_ = 0; j_ < 8; ++j_) *(LAS v2u*)(lds + (bo_) + bdst + 8 * j_ * XG_BP) = pk4(pb_[j_]); \
;             _Pragma("unroll") for (int j_ = 0; j_ < 8; ++j_) *(LAS v4u*)(lds + (bo_) + (arow + 32 * j_) * XG_AP + ach * 16) = pa_[j_]; } while (0)
; #define XG_STEP(t_, PBN, PAN, PBS, PAS) do { XG_ISSUE_A(PAN, (t_) + 2); { const int tb_ = ((t_) + 3 < NK) ? (t_) + 3 : NK - 1; XG_ISSUE_B(PBN, tb_); } \
;                 XG_STORE(PBS, PAS, (((t_) + 1) & 1) * XG_BUF); __syncthreads(); } while (0)
; template <bool UP>
; __device__ __forceinline__ void xgemm_unit(const Args& a, LAS unsigned char* lds, int e, int s, int cnt, int off_e, int rp, int tid, int lane, int wave) {
;     ...
;             __builtin_amdgcn_s_setprio(1);
;             int ras_ = 0; float rw_ = 0.f;
;             if (!UP) ras_ = LISTS[rp + ((tl < nrows) ? tl : nrows - 1)];
;             XG_ISSUE_A(pa0, 0); XG_ISSUE_B(pb0, 0); XG_ISSUE_A(pa1, 1); XG_ISSUE_B(pb1, 1); XG_ISSUE_B(pb2, 2);
;             XG_STORE(pb0, pa0, 0);
;             __syncthreads();
; #pragma unroll
;             for (int t = 0; t + 3 <= NK - 2; t += 3) {
;                 XG_STEP(t, pb0, pa2, pb1, pa1);
;                 if (!UP && t == 0) rw_ = RW[ras_];
;                 XG_STEP(t + 1, pb1, pa0, pb2, pa2);
;                 XG_STEP(t + 2, pb2, pa1, pb0, pa0);
	buffer_load_dwordx4 v[4:7], v14, s[8:11], s50 offen
	buffer_load_dwordx4 v[8:11], v18, s[8:11], s50 offen
	buffer_load_dwordx4 v[44:47], v22, s[8:11], s50 offen
	buffer_load_dwordx4 v[48:51], v26, s[8:11], s50 offen
	buffer_load_dwordx4 v[52:55], v30, s[8:11], s50 offen
	buffer_load_dwordx4 v[56:59], v34, s[8:11], s50 offen
	buffer_load_dwordx4 v[60:63], v38, s[8:11], s50 offen
	buffer_load_dwordx4 v[64:67], v42, s[8:11], s50 offen
	s_mov_b32 s0, 0x260000
	buffer_load_dwordx4 v[180:183], v2, s[12:15], s0 offen
	s_mov_b32 s0, 0x264000
	s_waitcnt vmcnt(32)
	v_cvt_pk_bf16_f32 v12, v212, v213
	v_cvt_pk_bf16_f32 v13, v214, v215
	buffer_load_dwordx4 v[184:187], v2, s[12:15], s0 offen
	s_mov_b32 s0, 0x268000
	ds_write_b64 v154, v[12:13] offset:58368
	s_waitcnt vmcnt(32)
	v_cvt_pk_bf16_f32 v12, v216, v217
	v_cvt_pk_bf16_f32 v13, v218, v219
	buffer_load_dwordx4 v[188:191], v2, s[12:15], s0 offen
	s_mov_b32 s0, 0x26c000
	ds_write_b64 v154, v[12:13] offset:60544
	s_waitcnt vmcnt(32)
	v_cvt_pk_bf16_f32 v12, v220, v221
	v_cvt_pk_bf16_f32 v13, v222, v223
	buffer_load_dwordx4 v[192:195], v2, s[12:15], s0 offen
	s_mov_b32 s0, 0x270000
	ds_write_b64 v154, v[12:13] offset:62720
	s_waitcnt vmcnt(32)
	v_cvt_pk_bf16_f32 v12, v224, v225
	v_cvt_pk_bf16_f32 v13, v226, v227
	buffer_load_dwordx4 v[196:199], v2, s[12:15], s0 offen
	s_mov_b32 s0, 0x274000
	ds_write_b64 v154, v[12:13] offset:64896
	s_waitcnt vmcnt(32)
	v_cvt_pk_bf16_f32 v12, v228, v229
	v_cvt_pk_bf16_f32 v13, v230, v231
	buffer_load_dwordx4 v[200:203], v2, s[12:15], s0 offen
	s_mov_b32 s0, 0x278000
	ds_write_b64 v155, v[12:13]
	s_waitcnt vmcnt(32)
	v_cvt_pk_bf16_f32 v12, v232, v233
	v_cvt_pk_bf16_f32 v13, v234, v235
	buffer_load_dwordx4 v[204:207], v2, s[12:15], s0 offen
	s_mov_b32 s0, 0x27c000
	ds_write_b64 v156, v[12:13]
	s_waitcnt vmcnt(32)
	v_cvt_pk_bf16_f32 v12, v236, v237
	v_cvt_pk_bf16_f32 v13, v238, v239
	buffer_load_dwordx4 v[208:211], v2, s[12:15], s0 offen
	ds_write_b64 v157, v[12:13]
	s_waitcnt vmcnt(32)
	v_cvt_pk_bf16_f32 v12, v240, v241
	v_cvt_pk_bf16_f32 v13, v242, v243
	ds_write_b64 v158, v[12:13]
	s_waitcnt vmcnt(31)
	ds_write_b128 v165, v[68:71] offset:58368
	s_waitcnt vmcnt(30)
	ds_write_b128 v165, v[72:75] offset:63488
	s_waitcnt vmcnt(29)
	ds_write_b128 v168, v[76:79] offset:58368
	s_waitcnt vmcnt(28)
	ds_write_b128 v166, v[80:83] offset:58368
	s_waitcnt vmcnt(27)
	ds_write_b128 v169, v[84:87] offset:58368
	s_waitcnt vmcnt(26)
	ds_write_b128 v169, v[88:91] offset:63488
	s_waitcnt vmcnt(25)
	ds_write_b128 v170, v[92:95] offset:63488
	s_waitcnt vmcnt(24)
	ds_write_b128 v167, v[96:99] offset:58368
	s_waitcnt lgkmcnt(0)
	s_barrier
	buffer_load_dwordx4 v[68:71], v14, s[8:11], s51 offen
	buffer_load_dwordx4 v[72:75], v18, s[8:11], s51 offen
	buffer_load_dwordx4 v[76:79], v22, s[8:11], s51 offen
	buffer_load_dwordx4 v[80:83], v26, s[8:11], s51 offen
	buffer_load_dwordx4 v[84:87], v30, s[8:11], s51 offen
	buffer_load_dwordx4 v[88:91], v34, s[8:11], s51 offen
	buffer_load_dwordx4 v[92:95], v38, s[8:11], s51 offen
	buffer_load_dwordx4 v[96:99], v42, s[8:11], s51 offen
	s_mov_b32 s0, 0x280000
	buffer_load_dwordx4 v[212:215], v2, s[12:15], s0 offen
	s_mov_b32 s0, 0x284000
	s_waitcnt vmcnt(32)
	v_cvt_pk_bf16_f32 v12, v100, v101
	v_cvt_pk_bf16_f32 v13, v102, v103
	buffer_load_dwordx4 v[216:219], v2, s[12:15], s0 offen
	s_mov_b32 s0, 0x288000
	ds_write_b64 v153, v[12:13] offset:40960
	s_waitcnt vmcnt(32)
	v_cvt_pk_bf16_f32 v12, v104, v105
	v_cvt_pk_bf16_f32 v13, v106, v107
	buffer_load_dwordx4 v[220:223], v2, s[12:15], s0 offen
	s_mov_b32 s0, 0x28c000
	ds_write_b64 v153, v[12:13] offset:43136
	s_waitcnt vmcnt(32)
	v_cvt_pk_bf16_f32 v12, v108, v109
	v_cvt_pk_bf16_f32 v13, v110, v111
	buffer_load_dwordx4 v[224:227], v2, s[12:15], s0 offen
	s_mov_b32 s0, 0x290000
	ds_write_b64 v153, v[12:13] offset:45312
	s_waitcnt vmcnt(32)
	v_cvt_pk_bf16_f32 v12, v112, v113
	v_cvt_pk_bf16_f32 v13, v114, v115
	buffer_load_dwordx4 v[228:231], v2, s[12:15], s0 offen
	s_mov_b32 s0, 0x294000
	ds_write_b64 v153, v[12:13] offset:47488
	s_waitcnt vmcnt(32)
	v_cvt_pk_bf16_f32 v12, v116, v117
	v_cvt_pk_bf16_f32 v13, v118, v119
	buffer_load_dwordx4 v[232:235], v2, s[12:15], s0 offen
	s_mov_b32 s0, 0x298000
	ds_write_b64 v153, v[12:13] offset:49664
	s_waitcnt vmcnt(32)
	v_cvt_pk_bf16_f32 v12, v120, v121
	v_cvt_pk_bf16_f32 v13, v122, v123
	buffer_load_dwordx4 v[236:239], v2, s[12:15], s0 offen
	s_mov_b32 s0, 0x29c000
	ds_write_b64 v153, v[12:13] offset:51840
	s_waitcnt vmcnt(32)
	v_cvt_pk_bf16_f32 v12, v124, v125
	v_cvt_pk_bf16_f32 v13, v126, v127
	buffer_load_dwordx4 v[240:243], v2, s[12:15], s0 offen
	ds_write_b64 v153, v[12:13] offset:54016
	s_waitcnt vmcnt(32)
	v_cvt_pk_bf16_f32 v12, v176, v177
	v_cvt_pk_bf16_f32 v13, v178, v179
	ds_write_b64 v153, v[12:13] offset:56192
	s_waitcnt vmcnt(31)
	ds_write_b128 v165, v[4:7]
	s_waitcnt vmcnt(30)
	ds_write_b128 v165, v[8:11] offset:5120
	s_waitcnt vmcnt(29)
	ds_write_b128 v165, v[44:47] offset:10240
	s_waitcnt vmcnt(28)
	ds_write_b128 v166, v[48:51]
	s_waitcnt vmcnt(27)
	ds_write_b128 v165, v[52:55] offset:20480
	s_waitcnt vmcnt(26)
	ds_write_b128 v165, v[56:59] offset:25600
	s_waitcnt vmcnt(25)
	ds_write_b128 v165, v[60:63] offset:30720
	s_waitcnt vmcnt(24)
	ds_write_b128 v167, v[64:67]
	s_waitcnt lgkmcnt(0)
	s_barrier
; #define XG_ISSUE_B(pb_, t_) do { _Pragma("unroll") for (int j_ = 0; j_ < 8; ++j_) pb_[j_] = __builtin_bit_cast(f32x4, __builtin_amdgcn_raw_buffer_load_b128(rB, boff, (64 * (t_) + 8 * j_) * LDB * 4, 0)); } while (0)
; #define XG_ISSUE_A(pa_, t_) do { _Pragma("unroll") for (int j_ = 0; j_ < 8; ++j_) pa_[j_] = __builtin_amdgcn_raw_buffer_load_b128(rA, aoff[j_], 128 * (t_), 0); } while (0)
; #define XG_STORE(pb_, pa_, bo_) do { _Pragma("unroll") for (int j_ = 0; j_ < 8; ++j_) *(LAS v2u*)(lds + (bo_) + bdst + 8 * j_ * XG_BP) = pk4(pb_[j_]); \
;             _Pragma("unroll") for (int j_ = 0; j_ < 8; ++j_) *(LAS v4u*)(lds + (bo_) + (arow + 32 * j_) * XG_AP + ach * 16) = pa_[j_]; } while (0)
; #define XG_STEP(t_, PBN, PAN, PBS, PAS) do { XG_ISSUE_A(PAN, (t_) + 2); { const int tb_ = ((t_) + 3 < NK) ? (t_) + 3 : NK - 1; XG_ISSUE_B(PBN, tb_); } \
;                 XG_STORE(PBS, PAS, (((t_) + 1) & 1) * XG_BUF); __syncthreads(); } while (0)
; template <bool UP>
; __device__ __forceinline__ void xgemm_unit(const Args& a, LAS unsigned char* lds, int e, int s, int cnt, int off_e, int rp, int tid, int lane, int wave) {
;     ...
;             __builtin_amdgcn_s_setprio(1);
;             int ras_ = 0; float rw_ = 0.f;
;             if (!UP) ras_ = LISTS[rp + ((tl < nrows) ? tl : nrows - 1)];
;             XG_ISSUE_A(pa0, 0); XG_ISSUE_B(pb0, 0); XG_ISSUE_A(pa1, 1); XG_ISSUE_B(pb1, 1); XG_ISSUE_B(pb2, 2);
;             XG_STORE(pb0, pa0, 0);
;             __syncthreads();
; #pragma unroll
;             for (int t = 0; t + 3 <= NK - 2; t += 3) {
;                 XG_STEP(t, pb0, pa2, pb1, pa1);
;                 if (!UP && t == 0) rw_ = RW[ras_];
;                 XG_STEP(t + 1, pb1, pa0, pb2, pa2);
;                 XG_STEP(t + 2, pb2, pa1, pb0, pa0);
	buffer_load_dwordx4 v[4:7], v14, s[8:11], s52 offen
	buffer_load_dwordx4 v[8:11], v18, s[8:11], s52 offen
	buffer_load_dwordx4 v[44:47], v22, s[8:11], s52 offen
	buffer_load_dwordx4 v[48:51], v26, s[8:11], s52 offen
	buffer_load_dwordx4 v[52:55], v30, s[8:11], s52 offen
	buffer_load_dwordx4 v[56:59], v34, s[8:11], s52 offen
	buffer_load_dwordx4 v[60:63], v38, s[8:11], s52 offen
	buffer_load_dwordx4 v[64:67], v42, s[8:11], s52 offen
	s_mov_b32 s0, 0x2a0000
	buffer_load_dwordx4 v[100:103], v2, s[12:15], s0 offen
	s_mov_b32 s0, 0x2a4000
	s_waitcnt vmcnt(32)
	v_cvt_pk_bf16_f32 v12, v180, v181
	v_cvt_pk_bf16_f32 v13, v182, v183
	buffer_load_dwordx4 v[104:107], v2, s[12:15], s0 offen
	s_mov_b32 s0, 0x2a8000
	ds_write_b64 v154, v[12:13] offset:58368
	s_waitcnt vmcnt(32)
	v_cvt_pk_bf16_f32 v12, v184, v185
	v_cvt_pk_bf16_f32 v13, v186, v187
	buffer_load_dwordx4 v[108:111], v2, s[12:15], s0 offen
	s_mov_b32 s0, 0x2ac000
	ds_write_b64 v154, v[12:13] offset:60544
	s_waitcnt vmcnt(32)
	v_cvt_pk_bf16_f32 v12, v188, v189
	v_cvt_pk_bf16_f32 v13, v190, v191
	buffer_load_dwordx4 v[112:115], v2, s[12:15], s0 offen
	s_mov_b32 s0, 0x2b0000
	ds_write_b64 v154, v[12:13] offset:62720
	s_waitcnt vmcnt(32)
	v_cvt_pk_bf16_f32 v12, v192, v193
	v_cvt_pk_bf16_f32 v13, v194, v195
	buffer_load_dwordx4 v[116:119], v2, s[12:15], s0 offen
	s_mov_b32 s0, 0x2b4000
	ds_write_b64 v154, v[12:13] offset:64896
	s_waitcnt vmcnt(32)
	v_cvt_pk_bf16_f32 v12, v196, v197
	v_cvt_pk_bf16_f32 v13, v198, v199
	buffer_load_dwordx4 v[120:123], v2, s[12:15], s0 offen
	s_mov_b32 s0, 0x2b8000
	ds_write_b64 v155, v[12:13]
	s_waitcnt vmcnt(32)
	v_cvt_pk_bf16_f32 v12, v200, v201
	v_cvt_pk_bf16_f32 v13, v202, v203
	buffer_load_dwordx4 v[124:127], v2, s[12:15], s0 offen
	s_mov_b32 s0, 0x2bc000
	ds_write_b64 v156, v[12:13]
	s_waitcnt vmcnt(32)
	v_cvt_pk_bf16_f32 v12, v204, v205
	v_cvt_pk_bf16_f32 v13, v206, v207
	buffer_load_dwordx4 v[176:179], v2, s[12:15], s0 offen
	ds_write_b64 v157, v[12:13]
	s_waitcnt vmcnt(32)
	v_cvt_pk_bf16_f32 v12, v208, v209
	v_cvt_pk_bf16_f32 v13, v210, v211
	ds_write_b64 v158, v[12:13]
	s_waitcnt vmcnt(31)
	ds_write_b128 v165, v[68:71] offset:58368
	s_waitcnt vmcnt(30)
	ds_write_b128 v165, v[72:75] offset:63488
	s_waitcnt vmcnt(29)
	ds_write_b128 v168, v[76:79] offset:58368
	s_waitcnt vmcnt(28)
	ds_write_b128 v166, v[80:83] offset:58368
	s_waitcnt vmcnt(27)
	ds_write_b128 v169, v[84:87] offset:58368
	s_waitcnt vmcnt(26)
	ds_write_b128 v169, v[88:91] offset:63488
	s_waitcnt vmcnt(25)
	ds_write_b128 v170, v[92:95] offset:63488
	s_waitcnt vmcnt(24)
	ds_write_b128 v167, v[96:99] offset:58368
	s_waitcnt lgkmcnt(0)
	s_barrier
	buffer_load_dwordx4 v[68:71], v14, s[8:11], s53 offen
	buffer_load_dwordx4 v[72:75], v18, s[8:11], s53 offen
	buffer_load_dwordx4 v[76:79], v22, s[8:11], s53 offen
	buffer_load_dwordx4 v[80:83], v26, s[8:11], s53 offen
	buffer_load_dwordx4 v[84:87], v30, s[8:11], s53 offen
	buffer_load_dwordx4 v[88:91], v34, s[8:11], s53 offen
	buffer_load_dwordx4 v[92:95], v38, s[8:11], s53 offen
	buffer_load_dwordx4 v[96:99], v42, s[8:11], s53 offen
	s_mov_b32 s0, 0x2c0000
	buffer_load_dwordx4 v[180:183], v2, s[12:15], s0 offen
	s_mov_b32 s0, 0x2c4000
	s_waitcnt vmcnt(32)
	v_cvt_pk_bf16_f32 v12, v212, v213
	v_cvt_pk_bf16_f32 v13, v214, v215
	buffer_load_dwordx4 v[184:187], v2, s[12:15], s0 offen
	s_mov_b32 s0, 0x2c8000
	ds_write_b64 v153, v[12:13] offset:40960
	s_waitcnt vmcnt(32)
	v_cvt_pk_bf16_f32 v12, v216, v217
	v_cvt_pk_bf16_f32 v13, v218, v219
	buffer_load_dwordx4 v[188:191], v2, s[12:15], s0 offen
	s_mov_b32 s0, 0x2cc000
	ds_write_b64 v153, v[12:13] offset:43136
	s_waitcnt vmcnt(32)
	v_cvt_pk_bf16_f32 v12, v220, v221
	v_cvt_pk_bf16_f32 v13, v222, v223
	buffer_load_dwordx4 v[192:195], v2, s[12:15], s0 offen
	s_mov_b32 s0, 0x2d0000
	ds_write_b64 v153, v[12:13] offset:45312
	s_waitcnt vmcnt(32)
	v_cvt_pk_bf16_f32 v12, v224, v225
	v_cvt_pk_bf16_f32 v13, v226, v227
	buffer_load_dwordx4 v[196:199], v2, s[12:15], s0 offen
	s_mov_b32 s0, 0x2d4000
	ds_write_b64 v153, v[12:13] offset:47488
	s_waitcnt vmcnt(32)
	v_cvt_pk_bf16_f32 v12, v228, v229
	v_cvt_pk_bf16_f32 v13, v230, v231
	buffer_load_dwordx4 v[200:203], v2, s[12:15], s0 offen
	s_mov_b32 s0, 0x2d8000
	ds_write_b64 v153, v[12:13] offset:49664
	s_waitcnt vmcnt(32)
	v_cvt_pk_bf16_f32 v12, v232, v233
	v_cvt_pk_bf16_f32 v13, v234, v235
	buffer_load_dwordx4 v[204:207], v2, s[12:15], s0 offen
	s_mov_b32 s0, 0x2dc000
	ds_write_b64 v153, v[12:13] offset:51840
	s_waitcnt vmcnt(32)
	v_cvt_pk_bf16_f32 v12, v236, v237
	v_cvt_pk_bf16_f32 v13, v238, v239
	buffer_load_dwordx4 v[208:211], v2, s[12:15], s0 offen
	ds_write_b64 v153, v[12:13] offset:54016
	s_waitcnt vmcnt(32)
	v_cvt_pk_bf16_f32 v12, v240, v241
	v_cvt_pk_bf16_f32 v13, v242, v243
	ds_write_b64 v153, v[12:13] offset:56192
	s_waitcnt vmcnt(31)
	ds_write_b128 v165, v[4:7]
	s_waitcnt vmcnt(30)
	ds_write_b128 v165, v[8:11] offset:5120
	s_waitcnt vmcnt(29)
	ds_write_b128 v165, v[44:47] offset:10240
	s_waitcnt vmcnt(28)
	ds_write_b128 v166, v[48:51]
	s_waitcnt vmcnt(27)
	ds_write_b128 v165, v[52:55] offset:20480
	s_waitcnt vmcnt(26)
	ds_write_b128 v165, v[56:59] offset:25600
	s_waitcnt vmcnt(25)
	ds_write_b128 v165, v[60:63] offset:30720
	s_waitcnt vmcnt(24)
	ds_write_b128 v167, v[64:67]
	s_waitcnt lgkmcnt(0)
	s_barrier
; #define XG_ISSUE_B(pb_, t_) do { _Pragma("unroll") for (int j_ = 0; j_ < 8; ++j_) pb_[j_] = __builtin_bit_cast(f32x4, __builtin_amdgcn_raw_buffer_load_b128(rB, boff, (64 * (t_) + 8 * j_) * LDB * 4, 0)); } while (0)
; #define XG_ISSUE_A(pa_, t_) do { _Pragma("unroll") for (int j_ = 0; j_ < 8; ++j_) pa_[j_] = __builtin_amdgcn_raw_buffer_load_b128(rA, aoff[j_], 128 * (t_), 0); } while (0)
; #define XG_STORE(pb_, pa_, bo_) do { _Pragma("unroll") for (int j_ = 0; j_ < 8; ++j_) *(LAS v2u*)(lds + (bo_) + bdst + 8 * j_ * XG_BP) = pk4(pb_[j_]); \
;             _Pragma("unroll") for (int j_ = 0; j_ < 8; ++j_) *(LAS v4u*)(lds + (bo_) + (arow + 32 * j_) * XG_AP + ach * 16) = pa_[j_]; } while (0)
; #define XG_STEP(t_, PBN, PAN, PBS, PAS) do { XG_ISSUE_A(PAN, (t_) + 2); { const int tb_ = ((t_) + 3 < NK) ? (t_) + 3 : NK - 1; XG_ISSUE_B(PBN, tb_); } \
;                 XG_STORE(PBS, PAS, (((t_) + 1) & 1) * XG_BUF); __syncthreads(); } while (0)
; template <bool UP>
; __device__ __forceinline__ void xgemm_unit(const Args& a, LAS unsigned char* lds, int e, int s, int cnt, int off_e, int rp, int tid, int lane, int wave) {
;     ...
;             __builtin_amdgcn_s_setprio(1);
;             int ras_ = 0; float rw_ = 0.f;
;             if (!UP) ras_ = LISTS[rp + ((tl < nrows) ? tl : nrows - 1)];
;             XG_ISSUE_A(pa0, 0); XG_ISSUE_B(pb0, 0); XG_ISSUE_A(pa1, 1); XG_ISSUE_B(pb1, 1); XG_ISSUE_B(pb2, 2);
;             XG_STORE(pb0, pa0, 0);
;             __syncthreads();
; #pragma unroll
;             for (int t = 0; t + 3 <= NK - 2; t += 3) {
;                 XG_STEP(t, pb0, pa2, pb1, pa1);
;                 if (!UP && t == 0) rw_ = RW[ras_];
;                 XG_STEP(t + 1, pb1, pa0, pb2, pa2);
;                 XG_STEP(t + 2, pb2, pa1, pb0, pa0);
	buffer_load_dwordx4 v[4:7], v14, s[8:11], s60 offen
	buffer_load_dwordx4 v[8:11], v18, s[8:11], s60 offen
	buffer_load_dwordx4 v[44:47], v22, s[8:11], s60 offen
	buffer_load_dwordx4 v[48:51], v26, s[8:11], s60 offen
	buffer_load_dwordx4 v[52:55], v30, s[8:11], s60 offen
	buffer_load_dwordx4 v[56:59], v34, s[8:11], s60 offen
	buffer_load_dwordx4 v[60:63], v38, s[8:11], s60 offen
	buffer_load_dwordx4 v[64:67], v42, s[8:11], s60 offen
	s_mov_b32 s0, 0x2e0000
	buffer_load_dwordx4 v[212:215], v2, s[12:15], s0 offen
	s_mov_b32 s0, 0x2e4000
	s_waitcnt vmcnt(32)
	v_cvt_pk_bf16_f32 v12, v100, v101
	v_cvt_pk_bf16_f32 v13, v102, v103
	buffer_load_dwordx4 v[216:219], v2, s[12:15], s0 offen
	s_mov_b32 s0, 0x2e8000
	ds_write_b64 v154, v[12:13] offset:58368
	s_waitcnt vmcnt(32)
	v_cvt_pk_bf16_f32 v12, v104, v105
	v_cvt_pk_bf16_f32 v13, v106, v107
	buffer_load_dwordx4 v[220:223], v2, s[12:15], s0 offen
	s_mov_b32 s0, 0x2ec000
	ds_write_b64 v154, v[12:13] offset:60544
	s_waitcnt vmcnt(32)
	v_cvt_pk_bf16_f32 v12, v108, v109
	v_cvt_pk_bf16_f32 v13, v110, v111
	buffer_load_dwordx4 v[224:227], v2, s[12:15], s0 offen
	s_mov_b32 s0, 0x2f0000
	ds_write_b64 v154, v[12:13] offset:62720
	s_waitcnt vmcnt(32)
	v_cvt_pk_bf16_f32 v12, v112, v113
	v_cvt_pk_bf16_f32 v13, v114, v115
	buffer_load_dwordx4 v[228:231], v2, s[12:15], s0 offen
	s_mov_b32 s0, 0x2f4000
	ds_write_b64 v154, v[12:13] offset:64896
	s_waitcnt vmcnt(32)
	v_cvt_pk_bf16_f32 v12, v116, v117
	v_cvt_pk_bf16_f32 v13, v118, v119
	buffer_load_dwordx4 v[232:235], v2, s[12:15], s0 offen
	s_mov_b32 s0, 0x2f8000
	ds_write_b64 v155, v[12:13]
	s_waitcnt vmcnt(32)
	v_cvt_pk_bf16_f32 v12, v120, v121
	v_cvt_pk_bf16_f32 v13, v122, v123
	buffer_load_dwordx4 v[236:239], v2, s[12:15], s0 offen
	s_mov_b32 s0, 0x2fc000
	ds_write_b64 v156, v[12:13]
	s_waitcnt vmcnt(32)
	v_cvt_pk_bf16_f32 v12, v124, v125
	v_cvt_pk_bf16_f32 v13, v126, v127
	buffer_load_dwordx4 v[240:243], v2, s[12:15], s0 offen
	ds_write_b64 v157, v[12:13]
	s_waitcnt vmcnt(32)
	v_cvt_pk_bf16_f32 v12, v176, v177
	v_cvt_pk_bf16_f32 v13, v178, v179
	ds_write_b64 v158, v[12:13]
	s_waitcnt vmcnt(31)
	ds_write_b128 v165, v[68:71] offset:58368
	s_waitcnt vmcnt(30)
	ds_write_b128 v165, v[72:75] offset:63488
	s_waitcnt vmcnt(29)
	ds_write_b128 v168, v[76:79] offset:58368
	s_waitcnt vmcnt(28)
	ds_write_b128 v166, v[80:83] offset:58368
	s_waitcnt vmcnt(27)
	ds_write_b128 v169, v[84:87] offset:58368
	s_waitcnt vmcnt(26)
	ds_write_b128 v169, v[88:91] offset:63488
	s_waitcnt vmcnt(25)
	ds_write_b128 v170, v[92:95] offset:63488
	s_waitcnt vmcnt(24)
	ds_write_b128 v167, v[96:99] offset:58368
	s_waitcnt lgkmcnt(0)
	s_barrier
	buffer_load_dwordx4 v[68:71], v14, s[8:11], s61 offen
	buffer_load_dwordx4 v[72:75], v18, s[8:11], s61 offen
	buffer_load_dwordx4 v[76:79], v22, s[8:11], s61 offen
	buffer_load_dwordx4 v[80:83], v26, s[8:11], s61 offen
	buffer_load_dwordx4 v[84:87], v30, s[8:11], s61 offen
	buffer_load_dwordx4 v[88:91], v34, s[8:11], s61 offen
	buffer_load_dwordx4 v[92:95], v38, s[8:11], s61 offen
	buffer_load_dwordx4 v[96:99], v42, s[8:11], s61 offen
	s_mov_b32 s0, 0x300000
	buffer_load_dwordx4 v[100:103], v2, s[12:15], s0 offen
	s_mov_b32 s0, 0x304000
	s_waitcnt vmcnt(32)
	v_cvt_pk_bf16_f32 v12, v180, v181
	v_cvt_pk_bf16_f32 v13, v182, v183
	buffer_load_dwordx4 v[104:107], v2, s[12:15], s0 offen
	s_mov_b32 s0, 0x308000
	ds_write_b64 v153, v[12:13] offset:40960
	s_waitcnt vmcnt(32)
	v_cvt_pk_bf16_f32 v12, v184, v185
	v_cvt_pk_bf16_f32 v13, v186, v187
	buffer_load_dwordx4 v[108:111], v2, s[12:15], s0 offen
	s_mov_b32 s0, 0x30c000
	ds_write_b64 v153, v[12:13] offset:43136
	s_waitcnt vmcnt(32)
	v_cvt_pk_bf16_f32 v12, v188, v189
	v_cvt_pk_bf16_f32 v13, v190, v191
	buffer_load_dwordx4 v[112:115], v2, s[12:15], s0 offen
	s_mov_b32 s0, 0x310000
	ds_write_b64 v153, v[12:13] offset:45312
	s_waitcnt vmcnt(32)
	v_cvt_pk_bf16_f32 v12, v192, v193
	v_cvt_pk_bf16_f32 v13, v194, v195
	buffer_load_dwordx4 v[116:119], v2, s[12:15], s0 offen
	s_mov_b32 s0, 0x314000
	ds_write_b64 v153, v[12:13] offset:47488
	s_waitcnt vmcnt(32)
	v_cvt_pk_bf16_f32 v12, v196, v197
	v_cvt_pk_bf16_f32 v13, v198, v199
	buffer_load_dwordx4 v[120:123], v2, s[12:15], s0 offen
	s_mov_b32 s0, 0x318000
	ds_write_b64 v153, v[12:13] offset:49664
	s_waitcnt vmcnt(32)
	v_cvt_pk_bf16_f32 v12, v200, v201
	v_cvt_pk_bf16_f32 v13, v202, v203
	buffer_load_dwordx4 v[124:127], v2, s[12:15], s0 offen
	s_mov_b32 s0, 0x31c000
	ds_write_b64 v153, v[12:13] offset:51840
	s_waitcnt vmcnt(32)
	v_cvt_pk_bf16_f32 v12, v204, v205
	v_cvt_pk_bf16_f32 v13, v206, v207
	buffer_load_dwordx4 v[176:179], v2, s[12:15], s0 offen
	ds_write_b64 v153, v[12:13] offset:54016
	s_waitcnt vmcnt(32)
	v_cvt_pk_bf16_f32 v12, v208, v209
	v_cvt_pk_bf16_f32 v13, v210, v211
	ds_write_b64 v153, v[12:13] offset:56192
	s_waitcnt vmcnt(31)
	ds_write_b128 v165, v[4:7]
	s_waitcnt vmcnt(30)
	ds_write_b128 v165, v[8:11] offset:5120
	s_waitcnt vmcnt(29)
	ds_write_b128 v165, v[44:47] offset:10240
	s_waitcnt vmcnt(28)
	ds_write_b128 v166, v[48:51]
	s_waitcnt vmcnt(27)
	ds_write_b128 v165, v[52:55] offset:20480
	s_waitcnt vmcnt(26)
	ds_write_b128 v165, v[56:59] offset:25600
	s_waitcnt vmcnt(25)
	ds_write_b128 v165, v[60:63] offset:30720
	s_waitcnt vmcnt(24)
	ds_write_b128 v167, v[64:67]
	s_waitcnt lgkmcnt(0)
	s_barrier
; #define XG_ISSUE_B(pb_, t_) do { _Pragma("unroll") for (int j_ = 0; j_ < 8; ++j_) pb_[j_] = __builtin_bit_cast(f32x4, __builtin_amdgcn_raw_buffer_load_b128(rB, boff, (64 * (t_) + 8 * j_) * LDB * 4, 0)); } while (0)
; #define XG_ISSUE_A(pa_, t_) do { _Pragma("unroll") for (int j_ = 0; j_ < 8; ++j_) pa_[j_] = __builtin_amdgcn_raw_buffer_load_b128(rA, aoff[j_], 128 * (t_), 0); } while (0)
; #define XG_STORE(pb_, pa_, bo_) do { _Pragma("unroll") for (int j_ = 0; j_ < 8; ++j_) *(LAS v2u*)(lds + (bo_) + bdst + 8 * j_ * XG_BP) = pk4(pb_[j_]); \
;             _Pragma("unroll") for (int j_ = 0; j_ < 8; ++j_) *(LAS v4u*)(lds + (bo_) + (arow + 32 * j_) * XG_AP + ach * 16) = pa_[j_]; } while (0)
; #define XG_STEP(t_, PBN, PAN, PBS, PAS) do { XG_ISSUE_A(PAN, (t_) + 2); { const int tb_ = ((t_) + 3 < NK) ? (t_) + 3 : NK - 1; XG_ISSUE_B(PBN, tb_); } \
;                 XG_STORE(PBS, PAS, (((t_) + 1) & 1) * XG_BUF); __syncthreads(); } while (0)
; template <bool UP>
; __device__ __forceinline__ void xgemm_unit(const Args& a, LAS unsigned char* lds, int e, int s, int cnt, int off_e, int rp, int tid, int lane, int wave) {
;     ...
;             __builtin_amdgcn_s_setprio(1);
;             int ras_ = 0; float rw_ = 0.f;
;             if (!UP) ras_ = LISTS[rp + ((tl < nrows) ? tl : nrows - 1)];
;             XG_ISSUE_A(pa0, 0); XG_ISSUE_B(pb0, 0); XG_ISSUE_A(pa1, 1); XG_ISSUE_B(pb1, 1); XG_ISSUE_B(pb2, 2);
;             XG_STORE(pb0, pa0, 0);
;             __syncthreads();
; #pragma unroll
;             for (int t = 0; t + 3 <= NK - 2; t += 3) {
;                 XG_STEP(t, pb0, pa2, pb1, pa1);
;                 if (!UP && t == 0) rw_ = RW[ras_];
;                 XG_STEP(t + 1, pb1, pa0, pb2, pa2);
;                 XG_STEP(t + 2, pb2, pa1, pb0, pa0);
	buffer_load_dwordx4 v[4:7], v14, s[8:11], s62 offen
	buffer_load_dwordx4 v[8:11], v18, s[8:11], s62 offen
	buffer_load_dwordx4 v[44:47], v22, s[8:11], s62 offen
	buffer_load_dwordx4 v[48:51], v26, s[8:11], s62 offen
	buffer_load_dwordx4 v[52:55], v30, s[8:11], s62 offen
	buffer_load_dwordx4 v[56:59], v34, s[8:11], s62 offen
	buffer_load_dwordx4 v[60:63], v38, s[8:11], s62 offen
	buffer_load_dwordx4 v[64:67], v42, s[8:11], s62 offen
	s_mov_b32 s0, 0x320000
	buffer_load_dwordx4 v[180:183], v2, s[12:15], s0 offen
	s_mov_b32 s0, 0x324000
	s_waitcnt vmcnt(32)
	v_cvt_pk_bf16_f32 v12, v212, v213
	v_cvt_pk_bf16_f32 v13, v214, v215
	buffer_load_dwordx4 v[184:187], v2, s[12:15], s0 offen
	s_mov_b32 s0, 0x328000
	ds_write_b64 v154, v[12:13] offset:58368
	s_waitcnt vmcnt(32)
	v_cvt_pk_bf16_f32 v12, v216, v217
	v_cvt_pk_bf16_f32 v13, v218, v219
	buffer_load_dwordx4 v[188:191], v2, s[12:15], s0 offen
	s_mov_b32 s0, 0x32c000
	ds_write_b64 v154, v[12:13] offset:60544
	s_waitcnt vmcnt(32)
	v_cvt_pk_bf16_f32 v12, v220, v221
	v_cvt_pk_bf16_f32 v13, v222, v223
	buffer_load_dwordx4 v[192:195], v2, s[12:15], s0 offen
	s_mov_b32 s0, 0x330000
	ds_write_b64 v154, v[12:13] offset:62720
	s_waitcnt vmcnt(32)
	v_cvt_pk_bf16_f32 v12, v224, v225
	v_cvt_pk_bf16_f32 v13, v226, v227
	buffer_load_dwordx4 v[196:199], v2, s[12:15], s0 offen
	s_mov_b32 s0, 0x334000
	ds_write_b64 v154, v[12:13] offset:64896
	s_waitcnt vmcnt(32)
	v_cvt_pk_bf16_f32 v12, v228, v229
	v_cvt_pk_bf16_f32 v13, v230, v231
	buffer_load_dwordx4 v[200:203], v2, s[12:15], s0 offen
	s_mov_b32 s0, 0x338000
	ds_write_b64 v155, v[12:13]
	s_waitcnt vmcnt(32)
	v_cvt_pk_bf16_f32 v12, v232, v233
	v_cvt_pk_bf16_f32 v13, v234, v235
	buffer_load_dwordx4 v[204:207], v2, s[12:15], s0 offen
	s_mov_b32 s0, 0x33c000
	ds_write_b64 v156, v[12:13]
	s_waitcnt vmcnt(32)
	v_cvt_pk_bf16_f32 v12, v236, v237
	v_cvt_pk_bf16_f32 v13, v238, v239
	buffer_load_dwordx4 v[208:211], v2, s[12:15], s0 offen
	ds_write_b64 v157, v[12:13]
	s_waitcnt vmcnt(32)
	v_cvt_pk_bf16_f32 v12, v240, v241
	v_cvt_pk_bf16_f32 v13, v242, v243
	ds_write_b64 v158, v[12:13]
	s_waitcnt vmcnt(31)
	ds_write_b128 v165, v[68:71] offset:58368
	s_waitcnt vmcnt(30)
	ds_write_b128 v165, v[72:75] offset:63488
	s_waitcnt vmcnt(29)
	ds_write_b128 v168, v[76:79] offset:58368
	s_waitcnt vmcnt(28)
	ds_write_b128 v166, v[80:83] offset:58368
	s_waitcnt vmcnt(27)
	ds_write_b128 v169, v[84:87] offset:58368
	s_waitcnt vmcnt(26)
	ds_write_b128 v169, v[88:91] offset:63488
	s_waitcnt vmcnt(25)
	ds_write_b128 v170, v[92:95] offset:63488
	s_waitcnt vmcnt(24)
	ds_write_b128 v167, v[96:99] offset:58368
	s_waitcnt lgkmcnt(0)
	s_barrier
	buffer_load_dwordx4 v[68:71], v14, s[8:11], s63 offen
	buffer_load_dwordx4 v[72:75], v18, s[8:11], s63 offen
	buffer_load_dwordx4 v[76:79], v22, s[8:11], s63 offen
	buffer_load_dwordx4 v[80:83], v26, s[8:11], s63 offen
	buffer_load_dwordx4 v[84:87], v30, s[8:11], s63 offen
	buffer_load_dwordx4 v[88:91], v34, s[8:11], s63 offen
	buffer_load_dwordx4 v[92:95], v38, s[8:11], s63 offen
	buffer_load_dwordx4 v[96:99], v42, s[8:11], s63 offen
	s_mov_b32 s0, 0x340000
	buffer_load_dwordx4 v[212:215], v2, s[12:15], s0 offen
	s_mov_b32 s0, 0x344000
	s_waitcnt vmcnt(32)
	v_cvt_pk_bf16_f32 v12, v100, v101
	v_cvt_pk_bf16_f32 v13, v102, v103
	buffer_load_dwordx4 v[216:219], v2, s[12:15], s0 offen
	s_mov_b32 s0, 0x348000
	ds_write_b64 v153, v[12:13] offset:40960
	s_waitcnt vmcnt(32)
	v_cvt_pk_bf16_f32 v12, v104, v105
	v_cvt_pk_bf16_f32 v13, v106, v107
	buffer_load_dwordx4 v[220:223], v2, s[12:15], s0 offen
	s_mov_b32 s0, 0x34c000
	ds_write_b64 v153, v[12:13] offset:43136
	s_waitcnt vmcnt(32)
	v_cvt_pk_bf16_f32 v12, v108, v109
	v_cvt_pk_bf16_f32 v13, v110, v111
	buffer_load_dwordx4 v[224:227], v2, s[12:15], s0 offen
	s_mov_b32 s0, 0x350000
	ds_write_b64 v153, v[12:13] offset:45312
	s_waitcnt vmcnt(32)
	v_cvt_pk_bf16_f32 v12, v112, v113
	v_cvt_pk_bf16_f32 v13, v114, v115
	buffer_load_dwordx4 v[228:231], v2, s[12:15], s0 offen
	s_mov_b32 s0, 0x354000
	ds_write_b64 v153, v[12:13] offset:47488
	s_waitcnt vmcnt(32)
	v_cvt_pk_bf16_f32 v12, v116, v117
	v_cvt_pk_bf16_f32 v13, v118, v119
	buffer_load_dwordx4 v[232:235], v2, s[12:15], s0 offen
	s_mov_b32 s0, 0x358000
	ds_write_b64 v153, v[12:13] offset:49664
	s_waitcnt vmcnt(32)
	v_cvt_pk_bf16_f32 v12, v120, v121
	v_cvt_pk_bf16_f32 v13, v122, v123
	buffer_load_dwordx4 v[236:239], v2, s[12:15], s0 offen
	s_mov_b32 s0, 0x35c000
	ds_write_b64 v153, v[12:13] offset:51840
	s_waitcnt vmcnt(32)
	v_cvt_pk_bf16_f32 v12, v124, v125
	v_cvt_pk_bf16_f32 v13, v126, v127
	buffer_load_dwordx4 v[240:243], v2, s[12:15], s0 offen
	ds_write_b64 v153, v[12:13] offset:54016
	s_waitcnt vmcnt(32)
	v_cvt_pk_bf16_f32 v12, v176, v177
	v_cvt_pk_bf16_f32 v13, v178, v179
	ds_write_b64 v153, v[12:13] offset:56192
	s_waitcnt vmcnt(31)
	ds_write_b128 v165, v[4:7]
	s_waitcnt vmcnt(30)
	ds_write_b128 v165, v[8:11] offset:5120
	s_waitcnt vmcnt(29)
	ds_write_b128 v165, v[44:47] offset:10240
	s_waitcnt vmcnt(28)
	ds_write_b128 v166, v[48:51]
	s_waitcnt vmcnt(27)
	ds_write_b128 v165, v[52:55] offset:20480
	s_waitcnt vmcnt(26)
	ds_write_b128 v165, v[56:59] offset:25600
	s_waitcnt vmcnt(25)
	ds_write_b128 v165, v[60:63] offset:30720
	s_waitcnt vmcnt(24)
	ds_write_b128 v167, v[64:67]
	s_waitcnt lgkmcnt(0)
	s_barrier
; #define XG_ISSUE_B(pb_, t_) do { _Pragma("unroll") for (int j_ = 0; j_ < 8; ++j_) pb_[j_] = __builtin_bit_cast(f32x4, __builtin_amdgcn_raw_buffer_load_b128(rB, boff, (64 * (t_) + 8 * j_) * LDB * 4, 0)); } while (0)
; #define XG_ISSUE_A(pa_, t_) do { _Pragma("unroll") for (int j_ = 0; j_ < 8; ++j_) pa_[j_] = __builtin_amdgcn_raw_buffer_load_b128(rA, aoff[j_], 128 * (t_), 0); } while (0)
; #define XG_STORE(pb_, pa_, bo_) do { _Pragma("unroll") for (int j_ = 0; j_ < 8; ++j_) *(LAS v2u*)(lds + (bo_) + bdst + 8 * j_ * XG_BP) = pk4(pb_[j_]); \
;             _Pragma("unroll") for (int j_ = 0; j_ < 8; ++j_) *(LAS v4u*)(lds + (bo_) + (arow + 32 * j_) * XG_AP + ach * 16) = pa_[j_]; } while (0)
; #define XG_STEP(t_, PBN, PAN, PBS, PAS) do { XG_ISSUE_A(PAN, (t_) + 2); { const int tb_ = ((t_) + 3 < NK) ? (t_) + 3 : NK - 1; XG_ISSUE_B(PBN, tb_); } \
;                 XG_STORE(PBS, PAS, (((t_) + 1) & 1) * XG_BUF); __syncthreads(); } while (0)
; template <bool UP>
; __device__ __forceinline__ void xgemm_unit(const Args& a, LAS unsigned char* lds, int e, int s, int cnt, int off_e, int rp, int tid, int lane, int wave) {
;     ...
;             __builtin_amdgcn_s_setprio(1);
;             int ras_ = 0; float rw_ = 0.f;
;             if (!UP) ras_ = LISTS[rp + ((tl < nrows) ? tl : nrows - 1)];
;             XG_ISSUE_A(pa0, 0); XG_ISSUE_B(pb0, 0); XG_ISSUE_A(pa1, 1); XG_ISSUE_B(pb1, 1); XG_ISSUE_B(pb2, 2);
;             XG_STORE(pb0, pa0, 0);
;             __syncthreads();
; #pragma unroll
;             for (int t = 0; t + 3 <= NK - 2; t += 3) {
;                 XG_STEP(t, pb0, pa2, pb1, pa1);
;                 if (!UP && t == 0) rw_ = RW[ras_];
;                 XG_STEP(t + 1, pb1, pa0, pb2, pa2);
;                 XG_STEP(t + 2, pb2, pa1, pb0, pa0);
	buffer_load_dwordx4 v[4:7], v14, s[8:11], s64 offen
	buffer_load_dwordx4 v[8:11], v18, s[8:11], s64 offen
	buffer_load_dwordx4 v[44:47], v22, s[8:11], s64 offen
	buffer_load_dwordx4 v[48:51], v26, s[8:11], s64 offen
	buffer_load_dwordx4 v[52:55], v30, s[8:11], s64 offen
	buffer_load_dwordx4 v[56:59], v34, s[8:11], s64 offen
	buffer_load_dwordx4 v[60:63], v38, s[8:11], s64 offen
	buffer_load_dwordx4 v[64:67], v42, s[8:11], s64 offen
	s_mov_b32 s0, 0x360000
	buffer_load_dwordx4 v[100:103], v2, s[12:15], s0 offen
	s_mov_b32 s0, 0x364000
	s_waitcnt vmcnt(32)
	v_cvt_pk_bf16_f32 v12, v180, v181
	v_cvt_pk_bf16_f32 v13, v182, v183
	buffer_load_dwordx4 v[104:107], v2, s[12:15], s0 offen
	s_mov_b32 s0, 0x368000
	ds_write_b64 v154, v[12:13] offset:58368
	s_waitcnt vmcnt(32)
	v_cvt_pk_bf16_f32 v12, v184, v185
	v_cvt_pk_bf16_f32 v13, v186, v187
	buffer_load_dwordx4 v[108:111], v2, s[12:15], s0 offen
	s_mov_b32 s0, 0x36c000
	ds_write_b64 v154, v[12:13] offset:60544
	s_waitcnt vmcnt(32)
	v_cvt_pk_bf16_f32 v12, v188, v189
	v_cvt_pk_bf16_f32 v13, v190, v191
	buffer_load_dwordx4 v[112:115], v2, s[12:15], s0 offen
	s_mov_b32 s0, 0x370000
	ds_write_b64 v154, v[12:13] offset:62720
	s_waitcnt vmcnt(32)
	v_cvt_pk_bf16_f32 v12, v192, v193
	v_cvt_pk_bf16_f32 v13, v194, v195
	buffer_load_dwordx4 v[116:119], v2, s[12:15], s0 offen
	s_mov_b32 s0, 0x374000
	ds_write_b64 v154, v[12:13] offset:64896
	s_waitcnt vmcnt(32)
	v_cvt_pk_bf16_f32 v12, v196, v197
	v_cvt_pk_bf16_f32 v13, v198, v199
	buffer_load_dwordx4 v[120:123], v2, s[12:15], s0 offen
	s_mov_b32 s0, 0x378000
	ds_write_b64 v155, v[12:13]
	s_waitcnt vmcnt(32)
	v_cvt_pk_bf16_f32 v12, v200, v201
	v_cvt_pk_bf16_f32 v13, v202, v203
	buffer_load_dwordx4 v[124:127], v2, s[12:15], s0 offen
	s_mov_b32 s0, 0x37c000
	ds_write_b64 v156, v[12:13]
	s_waitcnt vmcnt(32)
	v_cvt_pk_bf16_f32 v12, v204, v205
	v_cvt_pk_bf16_f32 v13, v206, v207
	buffer_load_dwordx4 v[176:179], v2, s[12:15], s0 offen
	ds_write_b64 v157, v[12:13]
	s_waitcnt vmcnt(32)
	v_cvt_pk_bf16_f32 v12, v208, v209
	v_cvt_pk_bf16_f32 v13, v210, v211
	ds_write_b64 v158, v[12:13]
	s_waitcnt vmcnt(31)
	ds_write_b128 v165, v[68:71] offset:58368
	s_waitcnt vmcnt(30)
	ds_write_b128 v165, v[72:75] offset:63488
	s_waitcnt vmcnt(29)
	ds_write_b128 v168, v[76:79] offset:58368
	s_waitcnt vmcnt(28)
	ds_write_b128 v166, v[80:83] offset:58368
	s_waitcnt vmcnt(27)
	ds_write_b128 v169, v[84:87] offset:58368
	s_waitcnt vmcnt(26)
	ds_write_b128 v169, v[88:91] offset:63488
	s_waitcnt vmcnt(25)
	ds_write_b128 v170, v[92:95] offset:63488
	s_waitcnt vmcnt(24)
	ds_write_b128 v167, v[96:99] offset:58368
	s_waitcnt lgkmcnt(0)
	s_barrier
	buffer_load_dwordx4 v[68:71], v14, s[8:11], s65 offen
	buffer_load_dwordx4 v[72:75], v18, s[8:11], s65 offen
	buffer_load_dwordx4 v[76:79], v22, s[8:11], s65 offen
	buffer_load_dwordx4 v[80:83], v26, s[8:11], s65 offen
	buffer_load_dwordx4 v[84:87], v30, s[8:11], s65 offen
	buffer_load_dwordx4 v[88:91], v34, s[8:11], s65 offen
	buffer_load_dwordx4 v[92:95], v38, s[8:11], s65 offen
	buffer_load_dwordx4 v[96:99], v42, s[8:11], s65 offen
	s_mov_b32 s0, 0x380000
	buffer_load_dwordx4 v[180:183], v2, s[12:15], s0 offen
	s_mov_b32 s0, 0x384000
	s_waitcnt vmcnt(32)
	v_cvt_pk_bf16_f32 v12, v212, v213
	v_cvt_pk_bf16_f32 v13, v214, v215
	buffer_load_dwordx4 v[184:187], v2, s[12:15], s0 offen
	s_mov_b32 s0, 0x388000
	ds_write_b64 v153, v[12:13] offset:40960
	s_waitcnt vmcnt(32)
	v_cvt_pk_bf16_f32 v12, v216, v217
	v_cvt_pk_bf16_f32 v13, v218, v219
	buffer_load_dwordx4 v[188:191], v2, s[12:15], s0 offen
	s_mov_b32 s0, 0x38c000
	ds_write_b64 v153, v[12:13] offset:43136
	s_waitcnt vmcnt(32)
	v_cvt_pk_bf16_f32 v12, v220, v221
	v_cvt_pk_bf16_f32 v13, v222, v223
	buffer_load_dwordx4 v[192:195], v2, s[12:15], s0 offen
	s_mov_b32 s0, 0x390000
	ds_write_b64 v153, v[12:13] offset:45312
	s_waitcnt vmcnt(32)
	v_cvt_pk_bf16_f32 v12, v224, v225
	v_cvt_pk_bf16_f32 v13, v226, v227
	buffer_load_dwordx4 v[196:199], v2, s[12:15], s0 offen
	s_mov_b32 s0, 0x394000
	ds_write_b64 v153, v[12:13] offset:47488
	s_waitcnt vmcnt(32)
	v_cvt_pk_bf16_f32 v12, v228, v229
	v_cvt_pk_bf16_f32 v13, v230, v231
	buffer_load_dwordx4 v[200:203], v2, s[12:15], s0 offen
	s_mov_b32 s0, 0x398000
	ds_write_b64 v153, v[12:13] offset:49664
	s_waitcnt vmcnt(32)
	v_cvt_pk_bf16_f32 v12, v232, v233
	v_cvt_pk_bf16_f32 v13, v234, v235
	buffer_load_dwordx4 v[204:207], v2, s[12:15], s0 offen
	s_mov_b32 s0, 0x39c000
	ds_write_b64 v153, v[12:13] offset:51840
	s_waitcnt vmcnt(32)
	v_cvt_pk_bf16_f32 v12, v236, v237
	v_cvt_pk_bf16_f32 v13, v238, v239
	buffer_load_dwordx4 v[208:211], v2, s[12:15], s0 offen
	ds_write_b64 v153, v[12:13] offset:54016
	s_waitcnt vmcnt(32)
	v_cvt_pk_bf16_f32 v12, v240, v241
	v_cvt_pk_bf16_f32 v13, v242, v243
	s_mov_b32 s0, 0x3a0000
	ds_write_b64 v153, v[12:13] offset:56192
	s_waitcnt vmcnt(31)
	ds_write_b128 v165, v[4:7]
	s_waitcnt vmcnt(30)
	ds_write_b128 v165, v[8:11] offset:5120
	s_waitcnt vmcnt(29)
	ds_write_b128 v165, v[44:47] offset:10240
	s_waitcnt vmcnt(28)
	ds_write_b128 v166, v[48:51]
	s_waitcnt vmcnt(27)
	ds_write_b128 v165, v[52:55] offset:20480
	s_waitcnt vmcnt(26)
	ds_write_b128 v165, v[56:59] offset:25600
	s_waitcnt vmcnt(25)
	ds_write_b128 v165, v[60:63] offset:30720
	s_waitcnt vmcnt(24)
	ds_write_b128 v167, v[64:67]
	s_waitcnt lgkmcnt(0)
	s_barrier
; #define XG_ISSUE_B(pb_, t_) do { _Pragma("unroll") for (int j_ = 0; j_ < 8; ++j_) pb_[j_] = __builtin_bit_cast(f32x4, __builtin_amdgcn_raw_buffer_load_b128(rB, boff, (64 * (t_) + 8 * j_) * LDB * 4, 0)); } while (0)
; #define XG_ISSUE_A(pa_, t_) do { _Pragma("unroll") for (int j_ = 0; j_ < 8; ++j_) pa_[j_] = __builtin_amdgcn_raw_buffer_load_b128(rA, aoff[j_], 128 * (t_), 0); } while (0)
; #define XG_STORE(pb_, pa_, bo_) do { _Pragma("unroll") for (int j_ = 0; j_ < 8; ++j_) *(LAS v2u*)(lds + (bo_) + bdst + 8 * j_ * XG_BP) = pk4(pb_[j_]); \
;             _Pragma("unroll") for (int j_ = 0; j_ < 8; ++j_) *(LAS v4u*)(lds + (bo_) + (arow + 32 * j_) * XG_AP + ach * 16) = pa_[j_]; } while (0)
; #define XG_STEP(t_, PBN, PAN, PBS, PAS) do { XG_ISSUE_A(PAN, (t_) + 2); { const int tb_ = ((t_) + 3 < NK) ? (t_) + 3 : NK - 1; XG_ISSUE_B(PBN, tb_); } \
;                 XG_STORE(PBS, PAS, (((t_) + 1) & 1) * XG_BUF); __syncthreads(); } while (0)
; template <bool UP>
; __device__ __forceinline__ void xgemm_unit(const Args& a, LAS unsigned char* lds, int e, int s, int cnt, int off_e, int rp, int tid, int lane, int wave) {
;     ...
;             __builtin_amdgcn_s_setprio(1);
;             int ras_ = 0; float rw_ = 0.f;
;             if (!UP) ras_ = LISTS[rp + ((tl < nrows) ? tl : nrows - 1)];
;             XG_ISSUE_A(pa0, 0); XG_ISSUE_B(pb0, 0); XG_ISSUE_A(pa1, 1); XG_ISSUE_B(pb1, 1); XG_ISSUE_B(pb2, 2);
;             XG_STORE(pb0, pa0, 0);
;             __syncthreads();
; #pragma unroll
;             for (int t = 0; t + 3 <= NK - 2; t += 3) {
;                 XG_STEP(t, pb0, pa2, pb1, pa1);
;                 if (!UP && t == 0) rw_ = RW[ras_];
;                 XG_STEP(t + 1, pb1, pa0, pb2, pa2);
;                 XG_STEP(t + 2, pb2, pa1, pb0, pa0);
	buffer_load_dwordx4 v[4:7], v14, s[8:11], s66 offen
	buffer_load_dwordx4 v[8:11], v18, s[8:11], s66 offen
	buffer_load_dwordx4 v[44:47], v22, s[8:11], s66 offen
	buffer_load_dwordx4 v[48:51], v26, s[8:11], s66 offen
	buffer_load_dwordx4 v[52:55], v30, s[8:11], s66 offen
	buffer_load_dwordx4 v[56:59], v34, s[8:11], s66 offen
	buffer_load_dwordx4 v[60:63], v38, s[8:11], s66 offen
	buffer_load_dwordx4 v[64:67], v42, s[8:11], s66 offen
	buffer_load_dwordx4 v[212:215], v2, s[12:15], s0 offen
	s_mov_b32 s0, 0x3a4000
	buffer_load_dwordx4 v[216:219], v2, s[12:15], s0 offen
	s_mov_b32 s0, 0x3a8000
	buffer_load_dwordx4 v[220:223], v2, s[12:15], s0 offen
	s_mov_b32 s0, 0x3ac000
	buffer_load_dwordx4 v[224:227], v2, s[12:15], s0 offen
	s_mov_b32 s0, 0x3b0000
	buffer_load_dwordx4 v[228:231], v2, s[12:15], s0 offen
	s_mov_b32 s0, 0x3b4000
	buffer_load_dwordx4 v[232:235], v2, s[12:15], s0 offen
	s_mov_b32 s0, 0x3b8000
	buffer_load_dwordx4 v[236:239], v2, s[12:15], s0 offen
	buffer_load_dwordx4 v[240:243], v2, s[12:15], s67 offen
	s_waitcnt vmcnt(39)
	v_cvt_pk_bf16_f32 v12, v100, v101
	v_cvt_pk_bf16_f32 v13, v102, v103
	ds_write_b64 v154, v[12:13] offset:58368
	s_waitcnt vmcnt(38)
	v_cvt_pk_bf16_f32 v12, v104, v105
	v_cvt_pk_bf16_f32 v13, v106, v107
	ds_write_b64 v154, v[12:13] offset:60544
	s_waitcnt vmcnt(37)
	v_cvt_pk_bf16_f32 v12, v108, v109
	v_cvt_pk_bf16_f32 v13, v110, v111
	ds_write_b64 v154, v[12:13] offset:62720
	s_waitcnt vmcnt(36)
	v_cvt_pk_bf16_f32 v12, v112, v113
	v_cvt_pk_bf16_f32 v13, v114, v115
	ds_write_b64 v154, v[12:13] offset:64896
	s_waitcnt vmcnt(35)
	v_cvt_pk_bf16_f32 v12, v116, v117
	v_cvt_pk_bf16_f32 v13, v118, v119
	ds_write_b64 v155, v[12:13]
	s_waitcnt vmcnt(34)
	v_cvt_pk_bf16_f32 v12, v120, v121
	v_cvt_pk_bf16_f32 v13, v122, v123
	ds_write_b64 v156, v[12:13]
	s_waitcnt vmcnt(33)
	v_cvt_pk_bf16_f32 v12, v124, v125
	v_cvt_pk_bf16_f32 v13, v126, v127
	ds_write_b64 v157, v[12:13]
	s_waitcnt vmcnt(32)
	v_cvt_pk_bf16_f32 v12, v176, v177
	v_cvt_pk_bf16_f32 v13, v178, v179
	ds_write_b64 v158, v[12:13]
	s_waitcnt vmcnt(31)
	ds_write_b128 v165, v[68:71] offset:58368
	s_waitcnt vmcnt(30)
	ds_write_b128 v165, v[72:75] offset:63488
	s_waitcnt vmcnt(29)
	ds_write_b128 v168, v[76:79] offset:58368
	s_waitcnt vmcnt(28)
	ds_write_b128 v166, v[80:83] offset:58368
	s_waitcnt vmcnt(27)
	ds_write_b128 v169, v[84:87] offset:58368
	s_waitcnt vmcnt(26)
	ds_write_b128 v169, v[88:91] offset:63488
	s_waitcnt vmcnt(25)
	ds_write_b128 v170, v[92:95] offset:63488
	s_waitcnt vmcnt(24)
	ds_write_b128 v167, v[96:99] offset:58368
	s_waitcnt lgkmcnt(0)
	s_barrier
	buffer_load_dwordx4 v[68:71], v14, s[8:11], s68 offen
	buffer_load_dwordx4 v[72:75], v18, s[8:11], s68 offen
	buffer_load_dwordx4 v[76:79], v22, s[8:11], s68 offen
	buffer_load_dwordx4 v[80:83], v26, s[8:11], s68 offen
	buffer_load_dwordx4 v[84:87], v30, s[8:11], s68 offen
	buffer_load_dwordx4 v[88:91], v34, s[8:11], s68 offen
	buffer_load_dwordx4 v[92:95], v38, s[8:11], s68 offen
	buffer_load_dwordx4 v[96:99], v42, s[8:11], s68 offen
	buffer_load_dwordx4 v[100:103], v2, s[12:15], s69 offen
	buffer_load_dwordx4 v[104:107], v2, s[12:15], s70 offen
	buffer_load_dwordx4 v[108:111], v2, s[12:15], s71 offen
	buffer_load_dwordx4 v[112:115], v2, s[12:15], s72 offen
	buffer_load_dwordx4 v[116:119], v2, s[12:15], s73 offen
	buffer_load_dwordx4 v[120:123], v2, s[12:15], s76 offen
	buffer_load_dwordx4 v[124:127], v2, s[12:15], s77 offen
	buffer_load_dwordx4 v[176:179], v2, s[12:15], s78 offen
	s_waitcnt vmcnt(39)
	v_cvt_pk_bf16_f32 v12, v180, v181
	v_cvt_pk_bf16_f32 v13, v182, v183
	ds_write_b64 v153, v[12:13] offset:40960
	s_waitcnt vmcnt(38)
	v_cvt_pk_bf16_f32 v12, v184, v185
	v_cvt_pk_bf16_f32 v13, v186, v187
	ds_write_b64 v153, v[12:13] offset:43136
	s_waitcnt vmcnt(37)
	v_cvt_pk_bf16_f32 v12, v188, v189
	v_cvt_pk_bf16_f32 v13, v190, v191
	ds_write_b64 v153, v[12:13] offset:45312
	s_waitcnt vmcnt(36)
	v_cvt_pk_bf16_f32 v12, v192, v193
	v_cvt_pk_bf16_f32 v13, v194, v195
	ds_write_b64 v153, v[12:13] offset:47488
	s_add_i32 s0, 0, 0xe400
	s_waitcnt vmcnt(35)
	v_cvt_pk_bf16_f32 v12, v196, v197
	v_cvt_pk_bf16_f32 v13, v198, v199
	ds_write_b64 v153, v[12:13] offset:49664
	s_waitcnt vmcnt(34)
	v_cvt_pk_bf16_f32 v12, v200, v201
	v_cvt_pk_bf16_f32 v13, v202, v203
	ds_write_b64 v153, v[12:13] offset:51840
	s_waitcnt vmcnt(33)
	v_cvt_pk_bf16_f32 v12, v204, v205
	v_cvt_pk_bf16_f32 v13, v206, v207
	ds_write_b64 v153, v[12:13] offset:54016
	s_waitcnt vmcnt(32)
	v_cvt_pk_bf16_f32 v12, v208, v209
	v_cvt_pk_bf16_f32 v13, v210, v211
	ds_write_b64 v153, v[12:13] offset:56192
	s_waitcnt vmcnt(31)
	ds_write_b128 v165, v[4:7]
	s_waitcnt vmcnt(30)
	ds_write_b128 v165, v[8:11] offset:5120
	s_waitcnt vmcnt(29)
	ds_write_b128 v165, v[44:47] offset:10240
	s_waitcnt vmcnt(28)
	ds_write_b128 v166, v[48:51]
	s_waitcnt vmcnt(27)
	ds_write_b128 v165, v[52:55] offset:20480
	s_waitcnt vmcnt(26)
	ds_write_b128 v165, v[56:59] offset:25600
	s_waitcnt vmcnt(25)
	ds_write_b128 v165, v[60:63] offset:30720
	s_waitcnt vmcnt(24)
	ds_write_b128 v167, v[64:67]
	s_waitcnt vmcnt(23)
	v_cvt_pk_bf16_f32 v16, v212, v213
	v_cvt_pk_bf16_f32 v17, v214, v215
	s_waitcnt lgkmcnt(0)
	s_barrier
; #define LAS __attribute__((address_space(3)))
; #define XG_ISSUE_B(pb_, t_) do { _Pragma("unroll") for (int j_ = 0; j_ < 8; ++j_) pb_[j_] = __builtin_bit_cast(f32x4, __builtin_amdgcn_raw_buffer_load_b128(rB, boff, (64 * (t_) + 8 * j_) * LDB * 4, 0)); } while (0)
; #define XG_ISSUE_A(pa_, t_) do { _Pragma("unroll") for (int j_ = 0; j_ < 8; ++j_) pa_[j_] = __builtin_amdgcn_raw_buffer_load_b128(rA, aoff[j_], 128 * (t_), 0); } while (0)
; #define XG_STORE(pb_, pa_, bo_) do { _Pragma("unroll") for (int j_ = 0; j_ < 8; ++j_) *(LAS v2u*)(lds + (bo_) + bdst + 8 * j_ * XG_BP) = pk4(pb_[j_]); \
;             _Pragma("unroll") for (int j_ = 0; j_ < 8; ++j_) *(LAS v4u*)(lds + (bo_) + (arow + 32 * j_) * XG_AP + ach * 16) = pa_[j_]; } while (0)
; #define XG_STEP(t_, PBN, PAN, PBS, PAS) do { XG_ISSUE_A(PAN, (t_) + 2); { const int tb_ = ((t_) + 3 < NK) ? (t_) + 3 : NK - 1; XG_ISSUE_B(PBN, tb_); } \
;                 XG_STORE(PBS, PAS, (((t_) + 1) & 1) * XG_BUF); __syncthreads(); } while (0)
; template <bool UP>
; __device__ __forceinline__ void xgemm_unit(const Args& a, LAS unsigned char* lds, int e, int s, int cnt, int off_e, int rp, int tid, int lane, int wave) {
;     ...
;             __builtin_amdgcn_s_setprio(1);
;             int ras_ = 0; float rw_ = 0.f;
;             if (!UP) ras_ = LISTS[rp + ((tl < nrows) ? tl : nrows - 1)];
;             XG_ISSUE_A(pa0, 0); XG_ISSUE_B(pb0, 0); XG_ISSUE_A(pa1, 1); XG_ISSUE_B(pb1, 1); XG_ISSUE_B(pb2, 2);
;             XG_STORE(pb0, pa0, 0);
;             __syncthreads();
; #pragma unroll
;             for (int t = 0; t + 3 <= NK - 2; t += 3) {
;                 XG_STEP(t, pb0, pa2, pb1, pa1);
;                 if (!UP && t == 0) rw_ = RW[ras_];
;                 XG_STEP(t + 1, pb1, pa0, pb2, pa2);
;                 XG_STEP(t + 2, pb2, pa1, pb0, pa0);
;                 if (!UP && t == 0) { LAS int* ri_ = (LAS int*)(lds + 2 * XG_BUF + 2048); ri_[2 * tl] = ras_; ri_[2 * tl + 1] = __float_as_int(rw_); }
;             }
;             XG_STORE(pb1, pa1, ((NK - 1) & 1) * XG_BUF); __syncthreads();
;             __syncthreads();
;             __builtin_amdgcn_s_setprio(0);
	buffer_load_dwordx4 v[46:49], v14, s[8:11], s79 offen
	buffer_load_dwordx4 v[50:53], v18, s[8:11], s79 offen
	buffer_load_dwordx4 v[54:57], v22, s[8:11], s79 offen
	buffer_load_dwordx4 v[58:61], v26, s[8:11], s79 offen
	buffer_load_dwordx4 v[62:65], v30, s[8:11], s79 offen
	buffer_load_dwordx4 v[180:183], v34, s[8:11], s79 offen
	buffer_load_dwordx4 v[184:187], v38, s[8:11], s79 offen
	buffer_load_dwordx4 v[188:191], v42, s[8:11], s79 offen
	buffer_load_dwordx4 v[192:195], v2, s[12:15], s80 offen
	buffer_load_dwordx4 v[196:199], v2, s[12:15], s81 offen
	buffer_load_dwordx4 v[200:203], v2, s[12:15], s82 offen
	buffer_load_dwordx4 v[204:207], v2, s[12:15], s83 offen
	buffer_load_dwordx4 v[208:211], v2, s[12:15], s84 offen
	buffer_load_dwordx4 v[10:13], v2, s[12:15], s85 offen
	buffer_load_dwordx4 v[6:9], v2, s[12:15], s86 offen
	s_nop 0
	buffer_load_dwordx4 v[2:5], v2, s[12:15], s87 offen
	ds_write_b64 v154, v[16:17] offset:58368
	s_waitcnt vmcnt(38)
	v_cvt_pk_bf16_f32 v16, v216, v217
	v_cvt_pk_bf16_f32 v17, v218, v219
	ds_write_b64 v154, v[16:17] offset:60544
	s_waitcnt vmcnt(37)
	v_cvt_pk_bf16_f32 v16, v220, v221
	v_cvt_pk_bf16_f32 v17, v222, v223
	ds_write_b64 v154, v[16:17] offset:62720
	s_waitcnt vmcnt(36)
	v_cvt_pk_bf16_f32 v16, v224, v225
	v_cvt_pk_bf16_f32 v17, v226, v227
	ds_write_b64 v154, v[16:17] offset:64896
	s_waitcnt vmcnt(35)
	v_cvt_pk_bf16_f32 v16, v228, v229
	v_cvt_pk_bf16_f32 v17, v230, v231
	ds_write_b64 v155, v[16:17]
	s_waitcnt vmcnt(34)
	v_cvt_pk_bf16_f32 v16, v232, v233
	v_cvt_pk_bf16_f32 v17, v234, v235
	ds_write_b64 v156, v[16:17]
	s_waitcnt vmcnt(33)
	v_cvt_pk_bf16_f32 v16, v236, v237
	v_cvt_pk_bf16_f32 v17, v238, v239
	ds_write_b64 v157, v[16:17]
	s_waitcnt vmcnt(32)
	v_cvt_pk_bf16_f32 v16, v240, v241
	v_cvt_pk_bf16_f32 v17, v242, v243
	ds_write_b64 v158, v[16:17]
	s_waitcnt vmcnt(31)
	ds_write_b128 v165, v[68:71] offset:58368
	s_waitcnt vmcnt(30)
	ds_write_b128 v165, v[72:75] offset:63488
	s_waitcnt vmcnt(29)
	ds_write_b128 v168, v[76:79] offset:58368
	s_waitcnt vmcnt(28)
	ds_write_b128 v166, v[80:83] offset:58368
	s_waitcnt vmcnt(27)
	ds_write_b128 v169, v[84:87] offset:58368
	s_waitcnt vmcnt(26)
	ds_write_b128 v169, v[88:91] offset:63488
	s_waitcnt vmcnt(25)
	ds_write_b128 v170, v[92:95] offset:63488
	s_waitcnt vmcnt(24)
	ds_write_b128 v167, v[96:99] offset:58368
	s_waitcnt lgkmcnt(0)
	s_barrier
	buffer_load_dwordx4 v[14:17], v14, s[8:11], s88 offen
	s_nop 0
	buffer_load_dwordx4 v[18:21], v18, s[8:11], s88 offen
	s_nop 0
	buffer_load_dwordx4 v[22:25], v22, s[8:11], s88 offen
	s_nop 0
	buffer_load_dwordx4 v[26:29], v26, s[8:11], s88 offen
	s_nop 0
	buffer_load_dwordx4 v[30:33], v30, s[8:11], s88 offen
	s_nop 0
	buffer_load_dwordx4 v[34:37], v34, s[8:11], s88 offen
	s_nop 0
	buffer_load_dwordx4 v[38:41], v38, s[8:11], s88 offen
	s_nop 0
	buffer_load_dwordx4 v[42:45], v42, s[8:11], s88 offen
	s_waitcnt vmcnt(31)
	v_cvt_pk_bf16_f32 v66, v100, v101
	v_cvt_pk_bf16_f32 v67, v102, v103
	ds_write_b64 v153, v[66:67] offset:40960
	s_waitcnt vmcnt(30)
	v_cvt_pk_bf16_f32 v66, v104, v105
	v_cvt_pk_bf16_f32 v67, v106, v107
	ds_write_b64 v153, v[66:67] offset:43136
	s_waitcnt vmcnt(29)
	v_cvt_pk_bf16_f32 v66, v108, v109
	v_cvt_pk_bf16_f32 v67, v110, v111
	ds_write_b64 v153, v[66:67] offset:45312
	s_waitcnt vmcnt(28)
	v_cvt_pk_bf16_f32 v66, v112, v113
	v_cvt_pk_bf16_f32 v67, v114, v115
	ds_write_b64 v153, v[66:67] offset:47488
	s_waitcnt vmcnt(27)
	v_cvt_pk_bf16_f32 v66, v116, v117
	v_cvt_pk_bf16_f32 v67, v118, v119
	ds_write_b64 v153, v[66:67] offset:49664
	s_waitcnt vmcnt(26)
	v_cvt_pk_bf16_f32 v66, v120, v121
	v_cvt_pk_bf16_f32 v67, v122, v123
	ds_write_b64 v153, v[66:67] offset:51840
	s_waitcnt vmcnt(25)
	v_cvt_pk_bf16_f32 v66, v124, v125
	v_cvt_pk_bf16_f32 v67, v126, v127
	ds_write_b64 v153, v[66:67] offset:54016
	s_waitcnt vmcnt(24)
	v_cvt_pk_bf16_f32 v66, v176, v177
	v_cvt_pk_bf16_f32 v67, v178, v179
	ds_write_b64 v153, v[66:67] offset:56192
	s_waitcnt vmcnt(23)
	ds_write_b128 v165, v[46:49]
	s_waitcnt vmcnt(22)
	ds_write_b128 v165, v[50:53] offset:5120
	s_waitcnt vmcnt(21)
	ds_write_b128 v165, v[54:57] offset:10240
	s_waitcnt vmcnt(20)
	ds_write_b128 v166, v[58:61]
	s_waitcnt vmcnt(19)
	ds_write_b128 v165, v[62:65] offset:20480
	s_waitcnt vmcnt(18)
	ds_write_b128 v165, v[180:183] offset:25600
	s_waitcnt vmcnt(17)
	ds_write_b128 v165, v[184:187] offset:30720
	s_waitcnt vmcnt(16)
	ds_write_b128 v167, v[188:191]
	s_waitcnt vmcnt(15)
	v_cvt_pk_bf16_f32 v46, v192, v193
	v_cvt_pk_bf16_f32 v47, v194, v195
	v_add_u32_e32 v48, 0, v152
	s_waitcnt lgkmcnt(0)
	s_barrier
	ds_write_b64 v48, v[46:47] offset:58368
	s_waitcnt vmcnt(14)
	v_cvt_pk_bf16_f32 v46, v196, v197
	v_cvt_pk_bf16_f32 v47, v198, v199
	ds_write_b64 v48, v[46:47] offset:60544
	s_waitcnt vmcnt(13)
	v_cvt_pk_bf16_f32 v46, v200, v201
	v_cvt_pk_bf16_f32 v47, v202, v203
	ds_write_b64 v48, v[46:47] offset:62720
	s_waitcnt vmcnt(12)
	v_cvt_pk_bf16_f32 v46, v204, v205
	v_cvt_pk_bf16_f32 v47, v206, v207
	ds_write_b64 v48, v[46:47] offset:64896
	s_waitcnt vmcnt(11)
	v_cvt_pk_bf16_f32 v46, v208, v209
	v_cvt_pk_bf16_f32 v47, v210, v211
	v_add_u32_e32 v48, s0, v152
	s_waitcnt vmcnt(10)
	v_cvt_pk_bf16_f32 v10, v10, v11
	v_cvt_pk_bf16_f32 v11, v12, v13
	s_waitcnt vmcnt(9)
	v_cvt_pk_bf16_f32 v6, v6, v7
	v_cvt_pk_bf16_f32 v7, v8, v9
	s_waitcnt vmcnt(8)
	v_cvt_pk_bf16_f32 v2, v2, v3
	v_cvt_pk_bf16_f32 v3, v4, v5
	ds_write_b64 v48, v[46:47] offset:8704
	ds_write_b64 v48, v[10:11] offset:10880
	ds_write_b64 v48, v[6:7] offset:13056
	ds_write_b64 v48, v[2:3] offset:15232
	s_waitcnt vmcnt(7)
	ds_write_b128 v165, v[14:17] offset:58368
	s_waitcnt vmcnt(6)
	ds_write_b128 v165, v[18:21] offset:63488
	s_waitcnt vmcnt(5)
	ds_write_b128 v168, v[22:25] offset:58368
	s_waitcnt vmcnt(4)
	ds_write_b128 v166, v[26:29] offset:58368
	s_waitcnt vmcnt(3)
	ds_write_b128 v169, v[30:33] offset:58368
	s_waitcnt vmcnt(2)
	ds_write_b128 v169, v[34:37] offset:63488
	s_waitcnt vmcnt(1)
	ds_write_b128 v170, v[38:41] offset:63488
	s_waitcnt vmcnt(0)
	ds_write_b128 v167, v[42:45] offset:58368
	s_waitcnt lgkmcnt(0)
	s_barrier
	s_barrier
	s_setprio 0
	s_branch .LBB0_1154

; __global__ void __launch_bounds__(NTHR, 2) fwd_kernel(Args args) {
	.amdhsa_kernel _Z10fwd_kernel4Args
		.amdhsa_group_segment_fixed_size 0
		.amdhsa_private_segment_fixed_size 0
		.amdhsa_kernarg_size 456
		.amdhsa_user_sgpr_count 2
		.amdhsa_user_sgpr_dispatch_ptr 0
		.amdhsa_user_sgpr_queue_ptr 0
		.amdhsa_user_sgpr_kernarg_segment_ptr 1
		.amdhsa_user_sgpr_dispatch_id 0
		.amdhsa_user_sgpr_kernarg_preload_length 0
		.amdhsa_user_sgpr_kernarg_preload_offset 0
		.amdhsa_user_sgpr_private_segment_size 0
		.amdhsa_uses_dynamic_stack 0
		.amdhsa_enable_private_segment 0
		.amdhsa_system_sgpr_workgroup_id_x 1
		.amdhsa_system_sgpr_workgroup_id_y 0
		.amdhsa_system_sgpr_workgroup_id_z 0
		.amdhsa_system_sgpr_workgroup_info 0
		.amdhsa_system_vgpr_workitem_id 0
		.amdhsa_next_free_vgpr 245
		.amdhsa_next_free_sgpr 98
		.amdhsa_accum_offset 248
		.amdhsa_reserve_vcc 1
		.amdhsa_float_round_mode_32 0
		.amdhsa_float_round_mode_16_64 0
		.amdhsa_float_denorm_mode_32 3
		.amdhsa_float_denorm_mode_16_64 3
		.amdhsa_dx10_clamp 1
		.amdhsa_ieee_mode 1
		.amdhsa_fp16_overflow 0
		.amdhsa_tg_split 0
		.amdhsa_exception_fp_ieee_invalid_op 0
		.amdhsa_exception_fp_denorm_src 0
		.amdhsa_exception_fp_ieee_div_zero 0
		.amdhsa_exception_fp_ieee_overflow 0
		.amdhsa_exception_fp_ieee_underflow 0
		.amdhsa_exception_fp_ieee_inexact 0
		.amdhsa_exception_int_div_zero 0
	.end_amdhsa_kernel

; __global__ void __launch_bounds__(NTHR, 2) fwd_kernel(Args args) {
amdhsa.kernels:
  - .agpr_count:     0
    .args:
      - .offset:         0
        .size:           200
        .value_kind:     by_value
      - .offset:         200
        .size:           4
        .value_kind:     hidden_block_count_x
      - .offset:         204
        .size:           4
        .value_kind:     hidden_block_count_y
      - .offset:         208
        .size:           4
        .value_kind:     hidden_block_count_z
      - .offset:         212
        .size:           2
        .value_kind:     hidden_group_size_x
      - .offset:         214
        .size:           2
        .value_kind:     hidden_group_size_y
      - .offset:         216
        .size:           2
        .value_kind:     hidden_group_size_z
      - .offset:         218
        .size:           2
        .value_kind:     hidden_remainder_x
      - .offset:         220
        .size:           2
        .value_kind:     hidden_remainder_y
      - .offset:         222
        .size:           2
        .value_kind:     hidden_remainder_z
      - .offset:         240
        .size:           8
        .value_kind:     hidden_global_offset_x
      - .offset:         248
        .size:           8
        .value_kind:     hidden_global_offset_y
      - .offset:         256
        .size:           8
        .value_kind:     hidden_global_offset_z
      - .offset:         264
        .size:           2
        .value_kind:     hidden_grid_dims
      - .offset:         320
        .size:           4
        .value_kind:     hidden_dynamic_lds_size
    .group_segment_fixed_size: 0
    .kernarg_segment_align: 8
    .kernarg_segment_size: 456
    .language:       OpenCL C
    .language_version:
      - 2
      - 0
    .max_flat_workgroup_size: 512
    .name:           _Z10fwd_kernel4Args
    .private_segment_fixed_size: 0
    .sgpr_count:     104
    .sgpr_spill_count: 24
    .symbol:         _Z10fwd_kernel4Args.kd
    .uniform_work_group_size: 1
    .uses_dynamic_stack: false
    .vgpr_count:     245
    .vgpr_spill_count: 0
    .wavefront_size: 64
